# fp8 GEMM K-loops of phases 2, 9, 10 re-cut: 16 MFMAs per barrier-delimited segment (8 barriers per two K-tiles instead of 16), same LDS-DMA order, counted vmcnt(8)
# speedup vs baseline: 1.0139x; 1.0139x over previous
.LBB0_215:
	ds_read_b128 v[10:13], v175
	ds_read_b128 v[14:17], v175 offset:1024
	ds_read_b128 v[166:169], v175 offset:2048
	ds_read_b128 v[170:173], v175 offset:3072
	s_add_u32 s28, s8, 0xfffc0080
	s_addc_u32 s29, s9, -1
	s_cmp_eq_u32 s64, 12
	s_cselect_b32 s31, s13, s29
	s_cselect_b32 s30, s21, s28
	s_cselect_b32 s29, s15, s63
	s_cselect_b32 s28, s51, s62
	s_mov_b32 m0, s52
	v_lshl_add_u64 v[2:3], s[8:9], 0, v[158:159]
	ds_read_b128 v[180:183], v176
	ds_read_b128 v[184:187], v176 offset:1024
	ds_read_b128 v[188:191], v176 offset:2048
	ds_read_b128 v[192:195], v176 offset:3072
	ds_read_b128 v[196:199], v176 offset:4096
	ds_read_b128 v[200:203], v176 offset:5120
	ds_read_b128 v[204:207], v176 offset:6144
	ds_read_b128 v[208:211], v176 offset:7168
	global_load_lds_dwordx4 v[2:3], off
	v_lshl_add_u64 v[2:3], s[8:9], 0, v[160:161]
	s_mov_b32 m0, s53
	s_nop 0
	global_load_lds_dwordx4 v[2:3], off
	ds_read_b128 v[212:215], v177
	ds_read_b128 v[216:219], v177 offset:1024
	ds_read_b128 v[220:223], v177 offset:2048
	ds_read_b128 v[224:227], v177 offset:3072
	s_waitcnt vmcnt(8) lgkmcnt(0)
	s_barrier
	s_setprio 1
	v_mfma_scale_f32_16x16x128_f8f6f4 v[138:141], v[10:17], v[180:187], v[138:141], v1, v1 op_sel_hi:[0,0,0]
	v_mfma_scale_f32_16x16x128_f8f6f4 v[134:137], v[166:173], v[180:187], v[134:137], v1, v1 op_sel_hi:[0,0,0]
	v_mfma_scale_f32_16x16x128_f8f6f4 v[122:125], v[10:17], v[188:195], v[122:125], v1, v1 op_sel_hi:[0,0,0]
	v_mfma_scale_f32_16x16x128_f8f6f4 v[118:121], v[166:173], v[188:195], v[118:121], v1, v1 op_sel_hi:[0,0,0]
	v_mfma_scale_f32_16x16x128_f8f6f4 v[98:101], v[10:17], v[196:203], v[98:101], v1, v1 op_sel_hi:[0,0,0]
	v_mfma_scale_f32_16x16x128_f8f6f4 v[90:93], v[166:173], v[196:203], v[90:93], v1, v1 op_sel_hi:[0,0,0]
	v_mfma_scale_f32_16x16x128_f8f6f4 v[70:73], v[10:17], v[204:211], v[70:73], v1, v1 op_sel_hi:[0,0,0]
	v_mfma_scale_f32_16x16x128_f8f6f4 v[58:61], v[166:173], v[204:211], v[58:61], v1, v1 op_sel_hi:[0,0,0]
	v_mfma_scale_f32_16x16x128_f8f6f4 v[146:149], v[212:219], v[180:187], v[146:149], v1, v1 op_sel_hi:[0,0,0]
	v_mfma_scale_f32_16x16x128_f8f6f4 v[142:145], v[220:227], v[180:187], v[142:145], v1, v1 op_sel_hi:[0,0,0]
	v_mfma_scale_f32_16x16x128_f8f6f4 v[130:133], v[212:219], v[188:195], v[130:133], v1, v1 op_sel_hi:[0,0,0]
	v_mfma_scale_f32_16x16x128_f8f6f4 v[126:129], v[220:227], v[188:195], v[126:129], v1, v1 op_sel_hi:[0,0,0]
	v_mfma_scale_f32_16x16x128_f8f6f4 v[114:117], v[212:219], v[196:203], v[114:117], v1, v1 op_sel_hi:[0,0,0]
	v_mfma_scale_f32_16x16x128_f8f6f4 v[110:113], v[220:227], v[196:203], v[110:113], v1, v1 op_sel_hi:[0,0,0]
	v_mfma_scale_f32_16x16x128_f8f6f4 v[82:85], v[212:219], v[204:211], v[82:85], v1, v1 op_sel_hi:[0,0,0]
	v_mfma_scale_f32_16x16x128_f8f6f4 v[78:81], v[220:227], v[204:211], v[78:81], v1, v1 op_sel_hi:[0,0,0]
	s_setprio 0
	s_barrier
	ds_read_b128 v[180:183], v176 offset:16384
	ds_read_b128 v[184:187], v176 offset:17408
	ds_read_b128 v[188:191], v176 offset:18432
	ds_read_b128 v[192:195], v176 offset:19456
	ds_read_b128 v[196:199], v176 offset:20480
	ds_read_b128 v[200:203], v176 offset:21504
	ds_read_b128 v[204:207], v176 offset:22528
	ds_read_b128 v[208:211], v176 offset:23552
	s_mov_b32 m0, s54
	v_lshl_add_u64 v[6:7], s[28:29], 0, v[154:155]
	global_load_lds_dwordx4 v[6:7], off
	v_lshl_add_u64 v[8:9], s[28:29], 0, v[150:151]
	s_mov_b32 m0, s55
	s_nop 0
	global_load_lds_dwordx4 v[8:9], off
	s_mov_b32 m0, s27
	v_lshl_add_u64 v[2:3], s[30:31], 0, v[156:157]
	global_load_lds_dwordx4 v[2:3], off
	v_lshl_add_u64 v[4:5], s[30:31], 0, v[152:153]
	s_mov_b32 m0, s41
	s_nop 0
	global_load_lds_dwordx4 v[4:5], off
	s_add_u32 s66, s28, 0x40000
	s_addc_u32 s67, s29, 0
	s_mov_b32 m0, s56
	v_lshl_add_u64 v[228:229], s[66:67], 0, v[154:155]
	global_load_lds_dwordx4 v[228:229], off
	v_lshl_add_u64 v[228:229], s[66:67], 0, v[150:151]
	s_mov_b32 m0, s57
	s_nop 0
	global_load_lds_dwordx4 v[228:229], off
	s_waitcnt vmcnt(8) lgkmcnt(0)
	s_barrier
	s_setprio 1
	v_mfma_scale_f32_16x16x128_f8f6f4 v[94:97], v[10:17], v[180:187], v[94:97], v1, v1 op_sel_hi:[0,0,0]
	v_mfma_scale_f32_16x16x128_f8f6f4 v[86:89], v[166:173], v[180:187], v[86:89], v1, v1 op_sel_hi:[0,0,0]
	v_mfma_scale_f32_16x16x128_f8f6f4 v[66:69], v[10:17], v[188:195], v[66:69], v1, v1 op_sel_hi:[0,0,0]
	v_mfma_scale_f32_16x16x128_f8f6f4 v[54:57], v[166:173], v[188:195], v[54:57], v1, v1 op_sel_hi:[0,0,0]
	v_mfma_scale_f32_16x16x128_f8f6f4 v[46:49], v[10:17], v[196:203], v[46:49], v1, v1 op_sel_hi:[0,0,0]
	v_mfma_scale_f32_16x16x128_f8f6f4 v[38:41], v[166:173], v[196:203], v[38:41], v1, v1 op_sel_hi:[0,0,0]
	v_mfma_scale_f32_16x16x128_f8f6f4 v[30:33], v[10:17], v[204:211], v[30:33], v1, v1 op_sel_hi:[0,0,0]
	v_mfma_scale_f32_16x16x128_f8f6f4 v[22:25], v[166:173], v[204:211], v[22:25], v1, v1 op_sel_hi:[0,0,0]
	v_mfma_scale_f32_16x16x128_f8f6f4 v[106:109], v[212:219], v[180:187], v[106:109], v1, v1 op_sel_hi:[0,0,0]
	v_mfma_scale_f32_16x16x128_f8f6f4 v[102:105], v[220:227], v[180:187], v[102:105], v1, v1 op_sel_hi:[0,0,0]
	v_mfma_scale_f32_16x16x128_f8f6f4 v[74:77], v[212:219], v[188:195], v[74:77], v1, v1 op_sel_hi:[0,0,0]
	v_mfma_scale_f32_16x16x128_f8f6f4 v[62:65], v[220:227], v[188:195], v[62:65], v1, v1 op_sel_hi:[0,0,0]
	v_mfma_scale_f32_16x16x128_f8f6f4 v[50:53], v[212:219], v[196:203], v[50:53], v1, v1 op_sel_hi:[0,0,0]
	v_mfma_scale_f32_16x16x128_f8f6f4 v[42:45], v[220:227], v[196:203], v[42:45], v1, v1 op_sel_hi:[0,0,0]
	v_mfma_scale_f32_16x16x128_f8f6f4 v[34:37], v[212:219], v[204:211], v[34:37], v1, v1 op_sel_hi:[0,0,0]
	v_mfma_scale_f32_16x16x128_f8f6f4 v[26:29], v[220:227], v[204:211], v[26:29], v1, v1 op_sel_hi:[0,0,0]
	s_setprio 0
	s_barrier
	ds_read_b128 v[10:13], v178
	ds_read_b128 v[14:17], v178 offset:1024
	ds_read_b128 v[166:169], v178 offset:2048
	ds_read_b128 v[170:173], v178 offset:3072
	s_add_u32 s30, s30, 0x40000
	s_addc_u32 s31, s31, 0
	s_mov_b32 m0, s42
	v_lshl_add_u64 v[212:213], s[30:31], 0, v[156:157]
	ds_read_b128 v[180:183], v176 offset:32768
	ds_read_b128 v[184:187], v176 offset:33792
	ds_read_b128 v[188:191], v176 offset:34816
	ds_read_b128 v[192:195], v176 offset:35840
	ds_read_b128 v[196:199], v176 offset:36864
	ds_read_b128 v[200:203], v176 offset:37888
	ds_read_b128 v[204:207], v176 offset:38912
	ds_read_b128 v[208:211], v176 offset:39936
	global_load_lds_dwordx4 v[212:213], off
	v_lshl_add_u64 v[212:213], s[30:31], 0, v[152:153]
	s_mov_b32 m0, s43
	s_nop 0
	global_load_lds_dwordx4 v[212:213], off
	ds_read_b128 v[212:215], v179
	ds_read_b128 v[216:219], v179 offset:1024
	ds_read_b128 v[220:223], v179 offset:2048
	ds_read_b128 v[224:227], v179 offset:3072
	s_waitcnt vmcnt(8) lgkmcnt(0)
	s_barrier
	s_setprio 1
	v_mfma_scale_f32_16x16x128_f8f6f4 v[138:141], v[10:17], v[180:187], v[138:141], v1, v1 op_sel_hi:[0,0,0]
	v_mfma_scale_f32_16x16x128_f8f6f4 v[134:137], v[166:173], v[180:187], v[134:137], v1, v1 op_sel_hi:[0,0,0]
	v_mfma_scale_f32_16x16x128_f8f6f4 v[122:125], v[10:17], v[188:195], v[122:125], v1, v1 op_sel_hi:[0,0,0]
	v_mfma_scale_f32_16x16x128_f8f6f4 v[118:121], v[166:173], v[188:195], v[118:121], v1, v1 op_sel_hi:[0,0,0]
	v_mfma_scale_f32_16x16x128_f8f6f4 v[98:101], v[10:17], v[196:203], v[98:101], v1, v1 op_sel_hi:[0,0,0]
	v_mfma_scale_f32_16x16x128_f8f6f4 v[90:93], v[166:173], v[196:203], v[90:93], v1, v1 op_sel_hi:[0,0,0]
	v_mfma_scale_f32_16x16x128_f8f6f4 v[70:73], v[10:17], v[204:211], v[70:73], v1, v1 op_sel_hi:[0,0,0]
	v_mfma_scale_f32_16x16x128_f8f6f4 v[58:61], v[166:173], v[204:211], v[58:61], v1, v1 op_sel_hi:[0,0,0]
	v_mfma_scale_f32_16x16x128_f8f6f4 v[146:149], v[212:219], v[180:187], v[146:149], v1, v1 op_sel_hi:[0,0,0]
	v_mfma_scale_f32_16x16x128_f8f6f4 v[142:145], v[220:227], v[180:187], v[142:145], v1, v1 op_sel_hi:[0,0,0]
	v_mfma_scale_f32_16x16x128_f8f6f4 v[130:133], v[212:219], v[188:195], v[130:133], v1, v1 op_sel_hi:[0,0,0]
	v_mfma_scale_f32_16x16x128_f8f6f4 v[126:129], v[220:227], v[188:195], v[126:129], v1, v1 op_sel_hi:[0,0,0]
	v_mfma_scale_f32_16x16x128_f8f6f4 v[114:117], v[212:219], v[196:203], v[114:117], v1, v1 op_sel_hi:[0,0,0]
	v_mfma_scale_f32_16x16x128_f8f6f4 v[110:113], v[220:227], v[196:203], v[110:113], v1, v1 op_sel_hi:[0,0,0]
	v_mfma_scale_f32_16x16x128_f8f6f4 v[82:85], v[212:219], v[204:211], v[82:85], v1, v1 op_sel_hi:[0,0,0]
	v_mfma_scale_f32_16x16x128_f8f6f4 v[78:81], v[220:227], v[204:211], v[78:81], v1, v1 op_sel_hi:[0,0,0]
	s_setprio 0
	s_barrier
	ds_read_b128 v[180:183], v176 offset:49152
	ds_read_b128 v[184:187], v176 offset:50176
	ds_read_b128 v[188:191], v176 offset:51200
	ds_read_b128 v[192:195], v176 offset:52224
	ds_read_b128 v[196:199], v176 offset:53248
	ds_read_b128 v[200:203], v176 offset:54272
	ds_read_b128 v[204:207], v176 offset:55296
	ds_read_b128 v[208:211], v176 offset:56320
	s_mov_b32 m0, s58
	v_lshl_add_u64 v[6:7], v[6:7], 0, s[4:5]
	global_load_lds_dwordx4 v[6:7], off
	v_lshl_add_u64 v[6:7], v[8:9], 0, s[4:5]
	s_mov_b32 m0, s59
	s_nop 0
	global_load_lds_dwordx4 v[6:7], off
	s_mov_b32 m0, s44
	v_lshl_add_u64 v[2:3], v[2:3], 0, s[4:5]
	global_load_lds_dwordx4 v[2:3], off
	v_lshl_add_u64 v[2:3], v[4:5], 0, s[4:5]
	s_mov_b32 m0, s45
	s_nop 0
	global_load_lds_dwordx4 v[2:3], off
	s_add_u32 s28, s28, 0x40080
	s_addc_u32 s29, s29, 0
	s_mov_b32 m0, s60
	v_lshl_add_u64 v[2:3], s[28:29], 0, v[154:155]
	global_load_lds_dwordx4 v[2:3], off
	v_lshl_add_u64 v[2:3], s[28:29], 0, v[150:151]
	s_mov_b32 m0, s61
	s_nop 0
	global_load_lds_dwordx4 v[2:3], off
	s_waitcnt vmcnt(8) lgkmcnt(0)
	s_barrier
	s_setprio 1
	v_mfma_scale_f32_16x16x128_f8f6f4 v[94:97], v[10:17], v[180:187], v[94:97], v1, v1 op_sel_hi:[0,0,0]
	v_mfma_scale_f32_16x16x128_f8f6f4 v[86:89], v[166:173], v[180:187], v[86:89], v1, v1 op_sel_hi:[0,0,0]
	v_mfma_scale_f32_16x16x128_f8f6f4 v[66:69], v[10:17], v[188:195], v[66:69], v1, v1 op_sel_hi:[0,0,0]
	v_mfma_scale_f32_16x16x128_f8f6f4 v[54:57], v[166:173], v[188:195], v[54:57], v1, v1 op_sel_hi:[0,0,0]
	v_mfma_scale_f32_16x16x128_f8f6f4 v[46:49], v[10:17], v[196:203], v[46:49], v1, v1 op_sel_hi:[0,0,0]
	v_mfma_scale_f32_16x16x128_f8f6f4 v[38:41], v[166:173], v[196:203], v[38:41], v1, v1 op_sel_hi:[0,0,0]
	v_mfma_scale_f32_16x16x128_f8f6f4 v[30:33], v[10:17], v[204:211], v[30:33], v1, v1 op_sel_hi:[0,0,0]
	v_mfma_scale_f32_16x16x128_f8f6f4 v[22:25], v[166:173], v[204:211], v[22:25], v1, v1 op_sel_hi:[0,0,0]
	v_mfma_scale_f32_16x16x128_f8f6f4 v[106:109], v[212:219], v[180:187], v[106:109], v1, v1 op_sel_hi:[0,0,0]
	v_mfma_scale_f32_16x16x128_f8f6f4 v[102:105], v[220:227], v[180:187], v[102:105], v1, v1 op_sel_hi:[0,0,0]
	v_mfma_scale_f32_16x16x128_f8f6f4 v[74:77], v[212:219], v[188:195], v[74:77], v1, v1 op_sel_hi:[0,0,0]
	v_mfma_scale_f32_16x16x128_f8f6f4 v[62:65], v[220:227], v[188:195], v[62:65], v1, v1 op_sel_hi:[0,0,0]
	v_mfma_scale_f32_16x16x128_f8f6f4 v[50:53], v[212:219], v[196:203], v[50:53], v1, v1 op_sel_hi:[0,0,0]
	v_mfma_scale_f32_16x16x128_f8f6f4 v[42:45], v[220:227], v[196:203], v[42:45], v1, v1 op_sel_hi:[0,0,0]
	v_mfma_scale_f32_16x16x128_f8f6f4 v[34:37], v[212:219], v[204:211], v[34:37], v1, v1 op_sel_hi:[0,0,0]
	v_mfma_scale_f32_16x16x128_f8f6f4 v[26:29], v[220:227], v[204:211], v[26:29], v1, v1 op_sel_hi:[0,0,0]
	s_setprio 0
	s_add_i32 s64, s64, 2
	s_add_u32 s8, s8, 0x100
	s_addc_u32 s9, s9, 0
	s_add_u32 s62, s62, 0x100
	s_addc_u32 s63, s63, 0
	s_cmp_gt_u32 s64, 13
	s_barrier
	s_cbranch_scc0 .LBB0_215
	v_mov_b32_e32 v166, v0
	s_nop 15
	s_nop 15
	s_lshl_b32 s9, s26, 8
	v_readfirstlane_b32 s8, v166
	s_ashr_i32 s13, s8, 2
	s_andn2_b32 s13, s13, 63
	s_lshr_b32 s8, s8, 1
	s_add_i32 s13, s13, s9
	s_and_b32 s8, s8, 0x60
	s_lshl_b32 s9, s50, 8
	v_and_or_b32 v178, v166, 15, s13
	v_lshrrev_b32_e32 v166, 1, v166
	s_or_b32 s8, s8, s9
	v_and_or_b32 v168, v166, 24, s8
	v_mov_b64_e32 v[14:15], v[18:19]
	v_mov_b64_e32 v[10:11], v[18:19]
	v_mov_b64_e32 v[6:7], v[18:19]
	v_mov_b64_e32 v[2:3], v[18:19]
	v_ashrrev_i32_e32 v169, 31, v168
	v_mov_b64_e32 v[166:167], s[2:3]
	v_mov_b64_e32 v[16:17], v[20:21]
	v_mov_b64_e32 v[12:13], v[20:21]
	v_mov_b64_e32 v[8:9], v[20:21]
	v_mov_b64_e32 v[4:5], v[20:21]
	v_mad_i64_i32 v[170:171], s[8:9], v178, s49, v[166:167]
	v_lshlrev_b64 v[168:169], 1, v[168:169]
	s_waitcnt vmcnt(6)
	v_lshl_add_u64 v[170:171], v[170:171], 0, v[168:169]
	v_pk_fma_f32 v[140:141], v[140:141], s[18:19], v[16:17] op_sel_hi:[1,0,1]
	v_pk_fma_f32 v[138:139], v[138:139], s[18:19], v[14:15] op_sel_hi:[1,0,1]
	v_pk_fma_f32 v[172:173], v[136:137], s[18:19], v[12:13] op_sel_hi:[1,0,1]
	v_pk_fma_f32 v[136:137], v[134:135], s[18:19], v[10:11] op_sel_hi:[1,0,1]
	v_cvt_pk_bf16_f32 v134, v138, v139
	v_cvt_pk_bf16_f32 v135, v140, v141
	v_pk_fma_f32 v[138:139], v[144:145], s[18:19], v[4:5] op_sel_hi:[1,0,1]
	v_cvt_pk_bf16_f32 v136, v136, v137
	v_cvt_pk_bf16_f32 v137, v172, v173
	global_store_dwordx4 v[170:171], v[134:137], off
	v_pk_fma_f32 v[140:141], v[142:143], s[18:19], v[2:3] op_sel_hi:[1,0,1]
	v_pk_fma_f32 v[124:125], v[124:125], s[18:19], v[16:17] op_sel_hi:[1,0,1]
	v_pk_fma_f32 v[134:135], v[146:147], s[18:19], v[6:7] op_sel_hi:[1,0,1]
	v_pk_fma_f32 v[136:137], v[148:149], s[18:19], v[8:9] op_sel_hi:[1,0,1]
	v_cvt_pk_bf16_f32 v134, v134, v135
	v_pk_fma_f32 v[122:123], v[122:123], s[18:19], v[14:15] op_sel_hi:[1,0,1]
	v_cvt_pk_bf16_f32 v135, v136, v137
	v_cvt_pk_bf16_f32 v136, v140, v141
	v_cvt_pk_bf16_f32 v137, v138, v139
	global_store_dwordx4 v[170:171], v[134:137], off offset:256
	v_pk_fma_f32 v[100:101], v[100:101], s[18:19], v[16:17] op_sel_hi:[1,0,1]
	v_pk_fma_f32 v[98:99], v[98:99], s[18:19], v[14:15] op_sel_hi:[1,0,1]
	v_or_b32_e32 v134, 16, v178
	v_mad_i64_i32 v[134:135], s[8:9], v134, s49, v[166:167]
	v_lshl_add_u64 v[134:135], v[134:135], 0, v[168:169]
	v_pk_fma_f32 v[136:137], v[120:121], s[18:19], v[12:13] op_sel_hi:[1,0,1]
	v_pk_fma_f32 v[120:121], v[118:119], s[18:19], v[10:11] op_sel_hi:[1,0,1]
	v_cvt_pk_bf16_f32 v118, v122, v123
	v_cvt_pk_bf16_f32 v119, v124, v125
	v_pk_fma_f32 v[122:123], v[128:129], s[18:19], v[4:5] op_sel_hi:[1,0,1]
	v_cvt_pk_bf16_f32 v120, v120, v121
	v_cvt_pk_bf16_f32 v121, v136, v137
	global_store_dwordx4 v[134:135], v[118:121], off
	v_pk_fma_f32 v[124:125], v[126:127], s[18:19], v[2:3] op_sel_hi:[1,0,1]
	v_pk_fma_f32 v[72:73], v[72:73], s[18:19], v[16:17] op_sel_hi:[1,0,1]
	v_pk_fma_f32 v[118:119], v[130:131], s[18:19], v[6:7] op_sel_hi:[1,0,1]
	v_pk_fma_f32 v[120:121], v[132:133], s[18:19], v[8:9] op_sel_hi:[1,0,1]
	v_cvt_pk_bf16_f32 v118, v118, v119
	v_pk_fma_f32 v[70:71], v[70:71], s[18:19], v[14:15] op_sel_hi:[1,0,1]
	v_cvt_pk_bf16_f32 v119, v120, v121
	v_cvt_pk_bf16_f32 v120, v124, v125
	v_cvt_pk_bf16_f32 v121, v122, v123
	global_store_dwordx4 v[134:135], v[118:121], off offset:256
	v_pk_fma_f32 v[66:67], v[66:67], s[18:19], v[14:15] op_sel_hi:[1,0,1]
	v_pk_fma_f32 v[62:63], v[62:63], s[18:19], v[2:3] op_sel_hi:[1,0,1]
	v_or_b32_e32 v118, 32, v178
	v_mad_i64_i32 v[118:119], s[8:9], v118, s49, v[166:167]
	v_lshl_add_u64 v[118:119], v[118:119], 0, v[168:169]
	v_pk_fma_f32 v[120:121], v[92:93], s[18:19], v[12:13] op_sel_hi:[1,0,1]
	v_pk_fma_f32 v[92:93], v[90:91], s[18:19], v[10:11] op_sel_hi:[1,0,1]
	v_cvt_pk_bf16_f32 v90, v98, v99
	v_cvt_pk_bf16_f32 v91, v100, v101
	v_pk_fma_f32 v[98:99], v[112:113], s[18:19], v[4:5] op_sel_hi:[1,0,1]
	v_cvt_pk_bf16_f32 v92, v92, v93
	v_cvt_pk_bf16_f32 v93, v120, v121
	global_store_dwordx4 v[118:119], v[90:93], off
	v_pk_fma_f32 v[100:101], v[110:111], s[18:19], v[2:3] op_sel_hi:[1,0,1]
	v_pk_fma_f32 v[48:49], v[48:49], s[18:19], v[16:17] op_sel_hi:[1,0,1]
	v_pk_fma_f32 v[90:91], v[114:115], s[18:19], v[6:7] op_sel_hi:[1,0,1]
	v_pk_fma_f32 v[92:93], v[116:117], s[18:19], v[8:9] op_sel_hi:[1,0,1]
	v_cvt_pk_bf16_f32 v90, v90, v91
	v_pk_fma_f32 v[46:47], v[46:47], s[18:19], v[14:15] op_sel_hi:[1,0,1]
	v_cvt_pk_bf16_f32 v91, v92, v93
	v_cvt_pk_bf16_f32 v92, v100, v101
	v_cvt_pk_bf16_f32 v93, v98, v99
	global_store_dwordx4 v[118:119], v[90:93], off offset:256
	v_pk_fma_f32 v[44:45], v[44:45], s[18:19], v[4:5] op_sel_hi:[1,0,1]
	v_pk_fma_f32 v[42:43], v[42:43], s[18:19], v[2:3] op_sel_hi:[1,0,1]
	v_or_b32_e32 v90, 48, v178
	v_mad_i64_i32 v[90:91], s[8:9], v90, s49, v[166:167]
	v_lshl_add_u64 v[90:91], v[90:91], 0, v[168:169]
	v_pk_fma_f32 v[92:93], v[60:61], s[18:19], v[12:13] op_sel_hi:[1,0,1]
	v_pk_fma_f32 v[60:61], v[58:59], s[18:19], v[10:11] op_sel_hi:[1,0,1]
	v_cvt_pk_bf16_f32 v58, v70, v71
	v_cvt_pk_bf16_f32 v59, v72, v73
	v_pk_fma_f32 v[70:71], v[80:81], s[18:19], v[4:5] op_sel_hi:[1,0,1]
	v_cvt_pk_bf16_f32 v60, v60, v61
	v_cvt_pk_bf16_f32 v61, v92, v93
	global_store_dwordx4 v[90:91], v[58:61], off
	v_pk_fma_f32 v[72:73], v[78:79], s[18:19], v[2:3] op_sel_hi:[1,0,1]
	v_pk_fma_f32 v[78:79], v[86:87], s[18:19], v[10:11] op_sel_hi:[1,0,1]
	v_pk_fma_f32 v[58:59], v[82:83], s[18:19], v[6:7] op_sel_hi:[1,0,1]
	v_pk_fma_f32 v[60:61], v[84:85], s[18:19], v[8:9] op_sel_hi:[1,0,1]
	v_cvt_pk_bf16_f32 v58, v58, v59
	v_pk_fma_f32 v[24:25], v[24:25], s[18:19], v[12:13] op_sel_hi:[1,0,1]
	v_cvt_pk_bf16_f32 v59, v60, v61
	v_cvt_pk_bf16_f32 v60, v72, v73
	v_cvt_pk_bf16_f32 v61, v70, v71
	global_store_dwordx4 v[90:91], v[58:61], off offset:256
	v_pk_fma_f32 v[72:73], v[88:89], s[18:19], v[12:13] op_sel_hi:[1,0,1]
	s_and_b64 vcc, exec, s[6:7]
	v_add_u32_e32 v58, 0x80, v178
	v_mad_i64_i32 v[58:59], s[8:9], v58, s49, v[166:167]
	v_lshl_add_u64 v[70:71], v[58:59], 0, v[168:169]
	v_pk_fma_f32 v[58:59], v[94:95], s[18:19], v[14:15] op_sel_hi:[1,0,1]
	v_pk_fma_f32 v[60:61], v[96:97], s[18:19], v[16:17] op_sel_hi:[1,0,1]
	v_cvt_pk_bf16_f32 v58, v58, v59
	v_pk_fma_f32 v[14:15], v[30:31], s[18:19], v[14:15] op_sel_hi:[1,0,1]
	v_cvt_pk_bf16_f32 v59, v60, v61
	v_cvt_pk_bf16_f32 v60, v78, v79
	v_cvt_pk_bf16_f32 v61, v72, v73
	global_store_dwordx4 v[70:71], v[58:61], off
	v_pk_fma_f32 v[72:73], v[104:105], s[18:19], v[4:5] op_sel_hi:[1,0,1]
	v_pk_fma_f32 v[78:79], v[102:103], s[18:19], v[2:3] op_sel_hi:[1,0,1]
	v_pk_fma_f32 v[58:59], v[106:107], s[18:19], v[6:7] op_sel_hi:[1,0,1]
	v_pk_fma_f32 v[60:61], v[108:109], s[18:19], v[8:9] op_sel_hi:[1,0,1]
	v_cvt_pk_bf16_f32 v58, v58, v59
	s_mov_b32 s50, s14
	v_cvt_pk_bf16_f32 v59, v60, v61
	v_cvt_pk_bf16_f32 v60, v78, v79
	v_cvt_pk_bf16_f32 v61, v72, v73
	global_store_dwordx4 v[70:71], v[58:61], off offset:256
	s_mov_b32 s26, s20
	s_mov_b64 s[28:29], s[24:25]
	v_add_u32_e32 v58, 0x90, v178
	v_mad_i64_i32 v[58:59], s[8:9], v58, s49, v[166:167]
	v_lshl_add_u64 v[58:59], v[58:59], 0, v[168:169]
	v_pk_fma_f32 v[60:61], v[68:69], s[18:19], v[16:17] op_sel_hi:[1,0,1]
	v_pk_fma_f32 v[68:69], v[56:57], s[18:19], v[12:13] op_sel_hi:[1,0,1]
	v_pk_fma_f32 v[56:57], v[54:55], s[18:19], v[10:11] op_sel_hi:[1,0,1]
	v_cvt_pk_bf16_f32 v54, v66, v67
	v_cvt_pk_bf16_f32 v55, v60, v61
	v_pk_fma_f32 v[60:61], v[64:65], s[18:19], v[4:5] op_sel_hi:[1,0,1]
	v_cvt_pk_bf16_f32 v56, v56, v57
	v_cvt_pk_bf16_f32 v57, v68, v69
	global_store_dwordx4 v[58:59], v[54:57], off
	v_pk_fma_f32 v[16:17], v[32:33], s[18:19], v[16:17] op_sel_hi:[1,0,1]
	s_mov_b64 s[30:31], s[22:23]
	v_pk_fma_f32 v[54:55], v[74:75], s[18:19], v[6:7] op_sel_hi:[1,0,1]
	v_pk_fma_f32 v[56:57], v[76:77], s[18:19], v[8:9] op_sel_hi:[1,0,1]
	v_cvt_pk_bf16_f32 v54, v54, v55
	v_readlane_b32 s72, v254, 51
	v_cvt_pk_bf16_f32 v55, v56, v57
	v_cvt_pk_bf16_f32 v56, v62, v63
	v_cvt_pk_bf16_f32 v57, v60, v61
	global_store_dwordx4 v[58:59], v[54:57], off offset:256
	v_readlane_b32 s73, v254, 52
	s_nop 0
	v_add_u32_e32 v54, 0xa0, v178
	v_mad_i64_i32 v[54:55], s[8:9], v54, s49, v[166:167]
	v_lshl_add_u64 v[54:55], v[54:55], 0, v[168:169]
	v_pk_fma_f32 v[56:57], v[40:41], s[18:19], v[12:13] op_sel_hi:[1,0,1]
	v_pk_fma_f32 v[40:41], v[38:39], s[18:19], v[10:11] op_sel_hi:[1,0,1]
	v_cvt_pk_bf16_f32 v38, v46, v47
	v_cvt_pk_bf16_f32 v39, v48, v49
	v_pk_fma_f32 v[12:13], v[22:23], s[18:19], v[10:11] op_sel_hi:[1,0,1]
	v_cvt_pk_bf16_f32 v40, v40, v41
	v_cvt_pk_bf16_f32 v41, v56, v57
	global_store_dwordx4 v[54:55], v[38:41], off
	s_nop 1
	v_pk_fma_f32 v[38:39], v[50:51], s[18:19], v[6:7] op_sel_hi:[1,0,1]
	v_pk_fma_f32 v[40:41], v[52:53], s[18:19], v[8:9] op_sel_hi:[1,0,1]
	v_cvt_pk_bf16_f32 v38, v38, v39
	v_pk_fma_f32 v[8:9], v[36:37], s[18:19], v[8:9] op_sel_hi:[1,0,1]
	v_cvt_pk_bf16_f32 v39, v40, v41
	v_cvt_pk_bf16_f32 v40, v42, v43
	v_cvt_pk_bf16_f32 v41, v44, v45
	global_store_dwordx4 v[54:55], v[38:41], off offset:256
	v_cvt_pk_bf16_f32 v10, v14, v15
	v_cvt_pk_bf16_f32 v11, v16, v17
	v_cvt_pk_bf16_f32 v12, v12, v13
	v_cvt_pk_bf16_f32 v13, v24, v25
	v_pk_fma_f32 v[6:7], v[34:35], s[18:19], v[6:7] op_sel_hi:[1,0,1]
	s_nop 0
	v_add_u32_e32 v38, 0xb0, v178
	v_mad_i64_i32 v[38:39], s[8:9], v38, s49, v[166:167]
	v_lshl_add_u64 v[38:39], v[38:39], 0, v[168:169]
	global_store_dwordx4 v[38:39], v[10:13], off
	s_nop 1
	v_pk_fma_f32 v[10:11], v[28:29], s[18:19], v[4:5] op_sel_hi:[1,0,1]
	v_pk_fma_f32 v[4:5], v[26:27], s[18:19], v[2:3] op_sel_hi:[1,0,1]
	v_cvt_pk_bf16_f32 v2, v6, v7
	v_cvt_pk_bf16_f32 v3, v8, v9
	s_nop 0
	v_cvt_pk_bf16_f32 v4, v4, v5
	v_cvt_pk_bf16_f32 v5, v10, v11
	global_store_dwordx4 v[38:39], v[2:5], off offset:256
	s_cbranch_vccz .LBB0_212
	s_waitcnt vmcnt(0)
	v_readlane_b32 s44, v254, 43
	v_readlane_b32 s45, v254, 44
	s_cmpk_gt_u32 s19, 0xff
	s_mov_b64 s[52:53], s[44:45]
	v_readlane_b32 s46, v254, 45
	v_readlane_b32 s47, v254, 46
	s_cbranch_scc1 .LBB0_219
	s_barrier

.LBB0_1442:
	s_add_u32 s48, s96, s46
	s_addc_u32 s49, s97, s47
	s_add_u32 s50, s48, 0x32370200
	ds_read_b128 v[188:191], v176
	ds_read_b128 v[192:195], v176 offset:1024
	ds_read_b128 v[196:199], v176 offset:2048
	ds_read_b128 v[200:203], v176 offset:3072
	s_addc_u32 s51, s49, 0
	s_add_u32 s81, s78, s46
	s_addc_u32 s82, s79, s47
	s_cmpk_eq_i32 s46, 0x600
	s_cselect_b64 vcc, -1, 0
	s_and_b64 s[48:49], vcc, exec
	v_cndmask_b32_e32 v166, v184, v180, vcc
	s_cselect_b32 s51, s11, s51
	s_cselect_b32 s50, s10, s50
	v_cndmask_b32_e32 v252, v172, v182, vcc
	v_cndmask_b32_e32 v169, v168, v181, vcc
	v_cndmask_b32_e32 v171, v170, v183, vcc
	s_cselect_b32 s49, s39, s82
	s_cselect_b32 s48, s41, s81
	s_mov_b32 m0, s45
	v_lshl_add_u64 v[6:7], v[4:5], 0, s[46:47]
	ds_read_b128 v[10:13], v177
	ds_read_b128 v[14:17], v177 offset:1024
	ds_read_b128 v[204:207], v177 offset:2048
	ds_read_b128 v[208:211], v177 offset:3072
	ds_read_b128 v[212:215], v177 offset:4096
	ds_read_b128 v[216:219], v177 offset:5120
	ds_read_b128 v[220:223], v177 offset:6144
	ds_read_b128 v[224:227], v177 offset:7168
	global_load_lds_dwordx4 v[6:7], off
	v_lshl_add_u64 v[6:7], v[2:3], 0, s[46:47]
	s_mov_b32 m0, s69
	s_nop 0
	global_load_lds_dwordx4 v[6:7], off
	ds_read_b128 v[228:231], v178
	ds_read_b128 v[232:235], v178 offset:1024
	ds_read_b128 v[236:239], v178 offset:2048
	ds_read_b128 v[240:243], v178 offset:3072
	s_waitcnt vmcnt(8) lgkmcnt(0)
	s_barrier
	s_setprio 1
	v_mfma_scale_f32_16x16x128_f8f6f4 v[154:157], v[188:195], v[10:17], v[154:157], v174, v174 op_sel_hi:[0,0,0]
	v_mfma_scale_f32_16x16x128_f8f6f4 v[146:149], v[196:203], v[10:17], v[146:149], v174, v174 op_sel_hi:[0,0,0]
	v_mfma_scale_f32_16x16x128_f8f6f4 v[138:141], v[188:195], v[204:211], v[138:141], v174, v174 op_sel_hi:[0,0,0]
	v_mfma_scale_f32_16x16x128_f8f6f4 v[130:133], v[196:203], v[204:211], v[130:133], v174, v174 op_sel_hi:[0,0,0]
	v_mfma_scale_f32_16x16x128_f8f6f4 v[122:125], v[188:195], v[212:219], v[122:125], v174, v174 op_sel_hi:[0,0,0]
	v_mfma_scale_f32_16x16x128_f8f6f4 v[114:117], v[196:203], v[212:219], v[114:117], v174, v174 op_sel_hi:[0,0,0]
	v_mfma_scale_f32_16x16x128_f8f6f4 v[106:109], v[188:195], v[220:227], v[106:109], v174, v174 op_sel_hi:[0,0,0]
	v_mfma_scale_f32_16x16x128_f8f6f4 v[90:93], v[196:203], v[220:227], v[90:93], v174, v174 op_sel_hi:[0,0,0]
	v_mfma_scale_f32_16x16x128_f8f6f4 v[158:161], v[228:235], v[10:17], v[158:161], v174, v174 op_sel_hi:[0,0,0]
	v_mfma_scale_f32_16x16x128_f8f6f4 v[150:153], v[236:243], v[10:17], v[150:153], v174, v174 op_sel_hi:[0,0,0]
	v_mfma_scale_f32_16x16x128_f8f6f4 v[142:145], v[228:235], v[204:211], v[142:145], v174, v174 op_sel_hi:[0,0,0]
	v_mfma_scale_f32_16x16x128_f8f6f4 v[134:137], v[236:243], v[204:211], v[134:137], v174, v174 op_sel_hi:[0,0,0]
	v_mfma_scale_f32_16x16x128_f8f6f4 v[126:129], v[228:235], v[212:219], v[126:129], v174, v174 op_sel_hi:[0,0,0]
	v_mfma_scale_f32_16x16x128_f8f6f4 v[118:121], v[236:243], v[212:219], v[118:121], v174, v174 op_sel_hi:[0,0,0]
	v_mfma_scale_f32_16x16x128_f8f6f4 v[110:113], v[228:235], v[220:227], v[110:113], v174, v174 op_sel_hi:[0,0,0]
	v_mfma_scale_f32_16x16x128_f8f6f4 v[98:101], v[236:243], v[220:227], v[98:101], v174, v174 op_sel_hi:[0,0,0]
	s_setprio 0
	s_barrier
	ds_read_b128 v[204:207], v177 offset:16384
	ds_read_b128 v[208:211], v177 offset:17408
	ds_read_b128 v[212:215], v177 offset:18432
	ds_read_b128 v[216:219], v177 offset:19456
	ds_read_b128 v[220:223], v177 offset:20480
	ds_read_b128 v[224:227], v177 offset:21504
	ds_read_b128 v[244:247], v177 offset:22528
	ds_read_b128 v[248:251], v177 offset:23552
	s_mov_b32 m0, s70
	v_lshl_add_u64 v[6:7], s[48:49], 0, v[162:163]
	global_load_lds_dwordx4 v[6:7], off
	v_lshl_add_u64 v[8:9], s[48:49], 0, v[164:165]
	s_mov_b32 m0, s71
	s_nop 0
	global_load_lds_dwordx4 v[8:9], off
	s_mov_b32 m0, s55
	s_nop 0
	global_load_lds_dwordx4 v166, s[50:51]
	s_mov_b32 m0, s56
	v_mov_b32_e32 v253, v167
	global_load_lds_dwordx4 v252, s[50:51]
	s_add_u32 s82, s48, 0x40000
	s_addc_u32 s83, s49, 0
	s_mov_b32 m0, s72
	v_lshl_add_u64 v[14:15], s[82:83], 0, v[162:163]
	global_load_lds_dwordx4 v[14:15], off
	v_lshl_add_u64 v[14:15], s[82:83], 0, v[164:165]
	s_mov_b32 m0, s73
	s_nop 0
	global_load_lds_dwordx4 v[14:15], off
	s_waitcnt vmcnt(8) lgkmcnt(0)
	s_barrier
	v_lshl_add_u64 v[12:13], s[50:51], 0, v[166:167]
	v_lshl_add_u64 v[10:11], s[50:51], 0, v[252:253]
	s_setprio 1
	v_mfma_scale_f32_16x16x128_f8f6f4 v[94:97], v[188:195], v[204:211], v[94:97], v174, v174 op_sel_hi:[0,0,0]
	v_mfma_scale_f32_16x16x128_f8f6f4 v[82:85], v[196:203], v[204:211], v[82:85], v174, v174 op_sel_hi:[0,0,0]
	v_mfma_scale_f32_16x16x128_f8f6f4 v[74:77], v[188:195], v[212:219], v[74:77], v174, v174 op_sel_hi:[0,0,0]
	v_mfma_scale_f32_16x16x128_f8f6f4 v[66:69], v[196:203], v[212:219], v[66:69], v174, v174 op_sel_hi:[0,0,0]
	v_mfma_scale_f32_16x16x128_f8f6f4 v[58:61], v[188:195], v[220:227], v[58:61], v174, v174 op_sel_hi:[0,0,0]
	v_mfma_scale_f32_16x16x128_f8f6f4 v[50:53], v[196:203], v[220:227], v[50:53], v174, v174 op_sel_hi:[0,0,0]
	v_mfma_scale_f32_16x16x128_f8f6f4 v[42:45], v[188:195], v[244:251], v[42:45], v174, v174 op_sel_hi:[0,0,0]
	v_mfma_scale_f32_16x16x128_f8f6f4 v[34:37], v[196:203], v[244:251], v[34:37], v174, v174 op_sel_hi:[0,0,0]
	v_mfma_scale_f32_16x16x128_f8f6f4 v[102:105], v[228:235], v[204:211], v[102:105], v174, v174 op_sel_hi:[0,0,0]
	v_mfma_scale_f32_16x16x128_f8f6f4 v[86:89], v[236:243], v[204:211], v[86:89], v174, v174 op_sel_hi:[0,0,0]
	v_mfma_scale_f32_16x16x128_f8f6f4 v[78:81], v[228:235], v[212:219], v[78:81], v174, v174 op_sel_hi:[0,0,0]
	v_mfma_scale_f32_16x16x128_f8f6f4 v[70:73], v[236:243], v[212:219], v[70:73], v174, v174 op_sel_hi:[0,0,0]
	v_mfma_scale_f32_16x16x128_f8f6f4 v[62:65], v[228:235], v[220:227], v[62:65], v174, v174 op_sel_hi:[0,0,0]
	v_mfma_scale_f32_16x16x128_f8f6f4 v[54:57], v[236:243], v[220:227], v[54:57], v174, v174 op_sel_hi:[0,0,0]
	v_mfma_scale_f32_16x16x128_f8f6f4 v[46:49], v[228:235], v[244:251], v[46:49], v174, v174 op_sel_hi:[0,0,0]
	v_mfma_scale_f32_16x16x128_f8f6f4 v[38:41], v[236:243], v[244:251], v[38:41], v174, v174 op_sel_hi:[0,0,0]
	s_setprio 0
	s_barrier
	ds_read_b128 v[188:191], v185
	ds_read_b128 v[192:195], v185 offset:1024
	ds_read_b128 v[196:199], v185 offset:2048
	ds_read_b128 v[200:203], v185 offset:3072
	s_mov_b32 m0, s57
	ds_read_b128 v[204:207], v177 offset:32768
	ds_read_b128 v[208:211], v177 offset:33792
	ds_read_b128 v[212:215], v177 offset:34816
	ds_read_b128 v[216:219], v177 offset:35840
	ds_read_b128 v[220:223], v177 offset:36864
	ds_read_b128 v[224:227], v177 offset:37888
	ds_read_b128 v[228:231], v177 offset:38912
	ds_read_b128 v[232:235], v177 offset:39936
	global_load_lds_dwordx4 v169, s[50:51]
	s_mov_b32 m0, s58
	s_nop 0
	global_load_lds_dwordx4 v171, s[50:51]
	ds_read_b128 v[236:239], v186
	ds_read_b128 v[240:243], v186 offset:1024
	ds_read_b128 v[244:247], v186 offset:2048
	ds_read_b128 v[248:251], v186 offset:3072
	s_waitcnt vmcnt(8) lgkmcnt(0)
	s_barrier
	s_setprio 1
	v_mfma_scale_f32_16x16x128_f8f6f4 v[154:157], v[188:195], v[204:211], v[154:157], v174, v174 op_sel_hi:[0,0,0]
	v_mfma_scale_f32_16x16x128_f8f6f4 v[146:149], v[196:203], v[204:211], v[146:149], v174, v174 op_sel_hi:[0,0,0]
	v_mfma_scale_f32_16x16x128_f8f6f4 v[138:141], v[188:195], v[212:219], v[138:141], v174, v174 op_sel_hi:[0,0,0]
	v_mfma_scale_f32_16x16x128_f8f6f4 v[130:133], v[196:203], v[212:219], v[130:133], v174, v174 op_sel_hi:[0,0,0]
	v_mfma_scale_f32_16x16x128_f8f6f4 v[122:125], v[188:195], v[220:227], v[122:125], v174, v174 op_sel_hi:[0,0,0]
	v_mfma_scale_f32_16x16x128_f8f6f4 v[114:117], v[196:203], v[220:227], v[114:117], v174, v174 op_sel_hi:[0,0,0]
	v_mfma_scale_f32_16x16x128_f8f6f4 v[106:109], v[188:195], v[228:235], v[106:109], v174, v174 op_sel_hi:[0,0,0]
	v_mfma_scale_f32_16x16x128_f8f6f4 v[90:93], v[196:203], v[228:235], v[90:93], v174, v174 op_sel_hi:[0,0,0]
	v_mfma_scale_f32_16x16x128_f8f6f4 v[158:161], v[236:243], v[204:211], v[158:161], v174, v174 op_sel_hi:[0,0,0]
	v_mfma_scale_f32_16x16x128_f8f6f4 v[150:153], v[244:251], v[204:211], v[150:153], v174, v174 op_sel_hi:[0,0,0]
	v_mfma_scale_f32_16x16x128_f8f6f4 v[142:145], v[236:243], v[212:219], v[142:145], v174, v174 op_sel_hi:[0,0,0]
	v_mfma_scale_f32_16x16x128_f8f6f4 v[134:137], v[244:251], v[212:219], v[134:137], v174, v174 op_sel_hi:[0,0,0]
	v_mfma_scale_f32_16x16x128_f8f6f4 v[126:129], v[236:243], v[220:227], v[126:129], v174, v174 op_sel_hi:[0,0,0]
	v_mfma_scale_f32_16x16x128_f8f6f4 v[118:121], v[244:251], v[220:227], v[118:121], v174, v174 op_sel_hi:[0,0,0]
	v_mfma_scale_f32_16x16x128_f8f6f4 v[110:113], v[236:243], v[228:235], v[110:113], v174, v174 op_sel_hi:[0,0,0]
	v_mfma_scale_f32_16x16x128_f8f6f4 v[98:101], v[244:251], v[228:235], v[98:101], v174, v174 op_sel_hi:[0,0,0]
	s_setprio 0
	s_barrier
	ds_read_b128 v[204:207], v177 offset:49152
	ds_read_b128 v[208:211], v177 offset:50176
	ds_read_b128 v[212:215], v177 offset:51200
	ds_read_b128 v[216:219], v177 offset:52224
	ds_read_b128 v[220:223], v177 offset:53248
	ds_read_b128 v[224:227], v177 offset:54272
	ds_read_b128 v[228:231], v177 offset:55296
	ds_read_b128 v[232:235], v177 offset:56320
	s_mov_b32 m0, s74
	v_lshl_add_u64 v[6:7], v[6:7], 0, s[18:19]
	global_load_lds_dwordx4 v[6:7], off
	v_lshl_add_u64 v[6:7], v[8:9], 0, s[18:19]
	s_mov_b32 m0, s75
	s_nop 0
	global_load_lds_dwordx4 v[6:7], off
	s_mov_b32 m0, s60
	v_lshl_add_u64 v[6:7], v[12:13], 0, s[18:19]
	global_load_lds_dwordx4 v[6:7], off
	v_lshl_add_u64 v[6:7], v[10:11], 0, s[18:19]
	s_mov_b32 m0, s61
	s_nop 0
	global_load_lds_dwordx4 v[6:7], off
	s_add_u32 s48, s48, 0x40080
	s_addc_u32 s49, s49, 0
	s_mov_b32 m0, s76
	v_lshl_add_u64 v[6:7], s[48:49], 0, v[162:163]
	global_load_lds_dwordx4 v[6:7], off
	v_lshl_add_u64 v[6:7], s[48:49], 0, v[164:165]
	s_mov_b32 m0, s77
	s_nop 0
	global_load_lds_dwordx4 v[6:7], off
	s_waitcnt vmcnt(8) lgkmcnt(0)
	s_barrier
	s_setprio 1
	v_mfma_scale_f32_16x16x128_f8f6f4 v[94:97], v[188:195], v[204:211], v[94:97], v174, v174 op_sel_hi:[0,0,0]
	v_mfma_scale_f32_16x16x128_f8f6f4 v[82:85], v[196:203], v[204:211], v[82:85], v174, v174 op_sel_hi:[0,0,0]
	v_mfma_scale_f32_16x16x128_f8f6f4 v[74:77], v[188:195], v[212:219], v[74:77], v174, v174 op_sel_hi:[0,0,0]
	v_mfma_scale_f32_16x16x128_f8f6f4 v[66:69], v[196:203], v[212:219], v[66:69], v174, v174 op_sel_hi:[0,0,0]
	v_mfma_scale_f32_16x16x128_f8f6f4 v[58:61], v[188:195], v[220:227], v[58:61], v174, v174 op_sel_hi:[0,0,0]
	v_mfma_scale_f32_16x16x128_f8f6f4 v[50:53], v[196:203], v[220:227], v[50:53], v174, v174 op_sel_hi:[0,0,0]
	v_mfma_scale_f32_16x16x128_f8f6f4 v[42:45], v[188:195], v[228:235], v[42:45], v174, v174 op_sel_hi:[0,0,0]
	v_mfma_scale_f32_16x16x128_f8f6f4 v[34:37], v[196:203], v[228:235], v[34:37], v174, v174 op_sel_hi:[0,0,0]
	v_mfma_scale_f32_16x16x128_f8f6f4 v[102:105], v[236:243], v[204:211], v[102:105], v174, v174 op_sel_hi:[0,0,0]
	v_mfma_scale_f32_16x16x128_f8f6f4 v[86:89], v[244:251], v[204:211], v[86:89], v174, v174 op_sel_hi:[0,0,0]
	v_mfma_scale_f32_16x16x128_f8f6f4 v[78:81], v[236:243], v[212:219], v[78:81], v174, v174 op_sel_hi:[0,0,0]
	v_mfma_scale_f32_16x16x128_f8f6f4 v[70:73], v[244:251], v[212:219], v[70:73], v174, v174 op_sel_hi:[0,0,0]
	v_mfma_scale_f32_16x16x128_f8f6f4 v[62:65], v[236:243], v[220:227], v[62:65], v174, v174 op_sel_hi:[0,0,0]
	v_mfma_scale_f32_16x16x128_f8f6f4 v[54:57], v[244:251], v[220:227], v[54:57], v174, v174 op_sel_hi:[0,0,0]
	v_mfma_scale_f32_16x16x128_f8f6f4 v[46:49], v[236:243], v[228:235], v[46:49], v174, v174 op_sel_hi:[0,0,0]
	v_mfma_scale_f32_16x16x128_f8f6f4 v[38:41], v[244:251], v[228:235], v[38:41], v174, v174 op_sel_hi:[0,0,0]
	s_setprio 0
	s_add_i32 s80, s80, 2
	s_add_u32 s46, s46, 0x100
	s_addc_u32 s47, s47, 0
	s_cmp_gt_u32 s80, 13
	s_barrier
	s_cbranch_scc0 .LBB0_1442
	v_mov_b32_e32 v2, v0
	s_nop 15
	s_nop 15
	s_waitcnt vmcnt(6)
	s_lshl_b32 s41, s68, 8
	v_readfirstlane_b32 s39, v2
	v_pk_fma_f32 v[10:11], v[154:155], s[30:31], v[30:31] op_sel_hi:[1,0,1]
	s_ashr_i32 s45, s39, 2
	v_min_f32_e32 v10, 0x40e00000, v10
	v_min_f32_e32 v11, 0x40e00000, v11
	s_andn2_b32 s45, s45, 63
	v_pk_mul_f32 v[12:13], v[10:11], s[34:35] op_sel_hi:[1,0]
	s_add_i32 s45, s45, s41
	v_exp_f32_e32 v12, v12
	v_exp_f32_e32 v13, v13
	v_and_or_b32 v6, v2, 15, s45
	v_lshrrev_b32_e32 v2, 1, v2
	v_and_b32_e32 v8, 24, v2
	v_pk_fma_f32 v[2:3], v[156:157], s[30:31], v[32:33] op_sel_hi:[1,0,1]
	v_pk_add_f32 v[12:13], v[12:13], 1.0 op_sel_hi:[1,0]
	v_min_f32_e32 v2, 0x40e00000, v2
	v_min_f32_e32 v3, 0x40e00000, v3
	v_pk_mul_f32 v[154:155], v[2:3], s[34:35] op_sel_hi:[1,0]
	v_rcp_f32_e32 v12, v12
	v_rcp_f32_e32 v13, v13
	v_exp_f32_e32 v154, v154
	v_exp_f32_e32 v155, v155
	v_pk_fma_f32 v[16:17], v[158:159], s[30:31], v[26:27] op_sel_hi:[1,0,1]
	v_pk_fma_f32 v[14:15], v[160:161], s[30:31], v[28:29] op_sel_hi:[1,0,1]
	v_med3_f32 v16, v16, s65, v179
	v_med3_f32 v17, v17, s65, v179
	v_pk_fma_f32 v[10:11], v[16:17], v[10:11], v[10:11]
	v_med3_f32 v14, v14, s65, v179
	v_med3_f32 v15, v15, s65, v179
	v_pk_mul_f32 v[10:11], v[10:11], v[12:13]
	v_pk_add_f32 v[12:13], v[154:155], 1.0 op_sel_hi:[1,0]
	v_pk_fma_f32 v[2:3], v[14:15], v[2:3], v[2:3]
	v_pk_fma_f32 v[14:15], v[146:147], s[30:31], v[22:23] op_sel_hi:[1,0,1]
	v_rcp_f32_e32 v12, v12
	v_rcp_f32_e32 v13, v13
	v_min_f32_e32 v14, 0x40e00000, v14
	v_min_f32_e32 v15, 0x40e00000, v15
	v_pk_mul_f32 v[146:147], v[14:15], s[34:35] op_sel_hi:[1,0]
	v_pk_mul_f32 v[2:3], v[2:3], v[12:13]
	v_exp_f32_e32 v146, v146
	v_exp_f32_e32 v147, v147
	v_pk_fma_f32 v[12:13], v[148:149], s[30:31], v[24:25] op_sel_hi:[1,0,1]
	v_pk_fma_f32 v[148:149], v[150:151], s[30:31], v[18:19] op_sel_hi:[1,0,1]
	v_min_f32_e32 v12, 0x40e00000, v12
	v_med3_f32 v148, v148, s65, v179
	v_med3_f32 v149, v149, s65, v179
	v_min_f32_e32 v13, 0x40e00000, v13
	v_pk_add_f32 v[146:147], v[146:147], 1.0 op_sel_hi:[1,0]
	v_pk_fma_f32 v[14:15], v[148:149], v[14:15], v[14:15]
	v_pk_mul_f32 v[148:149], v[12:13], s[34:35] op_sel_hi:[1,0]
	v_rcp_f32_e32 v146, v146
	v_rcp_f32_e32 v147, v147
	v_exp_f32_e32 v148, v148
	v_exp_f32_e32 v149, v149
	v_pk_fma_f32 v[16:17], v[152:153], s[30:31], v[20:21] op_sel_hi:[1,0,1]
	v_pk_mul_f32 v[14:15], v[14:15], v[146:147]
	v_med3_f32 v16, v16, s65, v179
	v_pk_add_f32 v[146:147], v[148:149], 1.0 op_sel_hi:[1,0]
	v_mov_b32_e32 v149, v167
	v_cvt_pk_fp8_f32 v149, v14, v15
	v_pk_fma_f32 v[14:15], v[138:139], s[30:31], v[30:31] op_sel_hi:[1,0,1]
	v_med3_f32 v17, v17, s65, v179
	v_mov_b32_e32 v148, v167
	v_min_f32_e32 v14, 0x40e00000, v14
	v_min_f32_e32 v15, 0x40e00000, v15
	v_cvt_pk_fp8_f32 v148, v10, v11
	v_pk_fma_f32 v[10:11], v[16:17], v[12:13], v[12:13]
	v_pk_mul_f32 v[16:17], v[14:15], s[34:35] op_sel_hi:[1,0]
	v_pk_fma_f32 v[12:13], v[140:141], s[30:31], v[32:33] op_sel_hi:[1,0,1]
	v_exp_f32_e32 v16, v16
	v_exp_f32_e32 v17, v17
	v_min_f32_e32 v12, 0x40e00000, v12
	v_min_f32_e32 v13, 0x40e00000, v13
	v_pk_fma_f32 v[140:141], v[142:143], s[30:31], v[26:27] op_sel_hi:[1,0,1]
	v_pk_add_f32 v[16:17], v[16:17], 1.0 op_sel_hi:[1,0]
	v_pk_mul_f32 v[142:143], v[12:13], s[34:35] op_sel_hi:[1,0]
	v_rcp_f32_e32 v16, v16
	v_rcp_f32_e32 v17, v17
	v_exp_f32_e32 v142, v142
	v_exp_f32_e32 v143, v143
	v_med3_f32 v140, v140, s65, v179
	v_med3_f32 v141, v141, s65, v179
	v_pk_fma_f32 v[14:15], v[140:141], v[14:15], v[14:15]
	v_pk_fma_f32 v[138:139], v[144:145], s[30:31], v[28:29] op_sel_hi:[1,0,1]
	v_pk_mul_f32 v[14:15], v[14:15], v[16:17]
	v_pk_add_f32 v[16:17], v[142:143], 1.0 op_sel_hi:[1,0]
	v_med3_f32 v138, v138, s65, v179
	v_rcp_f32_e32 v16, v16
	v_rcp_f32_e32 v17, v17
	v_med3_f32 v139, v139, s65, v179
	v_pk_fma_f32 v[130:131], v[130:131], s[30:31], v[22:23] op_sel_hi:[1,0,1]
	v_pk_fma_f32 v[12:13], v[138:139], v[12:13], v[12:13]
	v_min_f32_e32 v130, 0x40e00000, v130
	v_min_f32_e32 v131, 0x40e00000, v131
	v_pk_mul_f32 v[12:13], v[12:13], v[16:17]
	v_pk_fma_f32 v[16:17], v[132:133], s[30:31], v[24:25] op_sel_hi:[1,0,1]
	v_pk_fma_f32 v[132:133], v[136:137], s[30:31], v[20:21] op_sel_hi:[1,0,1]
	v_pk_mul_f32 v[136:137], v[130:131], s[34:35] op_sel_hi:[1,0]
	v_pk_fma_f32 v[134:135], v[134:135], s[30:31], v[18:19] op_sel_hi:[1,0,1]
	v_exp_f32_e32 v136, v136
	v_exp_f32_e32 v137, v137
	v_med3_f32 v134, v134, s65, v179
	v_med3_f32 v135, v135, s65, v179
	v_min_f32_e32 v16, 0x40e00000, v16
	v_min_f32_e32 v17, 0x40e00000, v17
	v_pk_fma_f32 v[130:131], v[134:135], v[130:131], v[130:131]
	v_pk_mul_f32 v[134:135], v[16:17], s[34:35] op_sel_hi:[1,0]
	v_pk_add_f32 v[136:137], v[136:137], 1.0 op_sel_hi:[1,0]
	v_exp_f32_e32 v134, v134
	v_exp_f32_e32 v135, v135
	v_rcp_f32_e32 v136, v136
	v_rcp_f32_e32 v137, v137
	v_med3_f32 v132, v132, s65, v179
	v_pk_add_f32 v[134:135], v[134:135], 1.0 op_sel_hi:[1,0]
	v_med3_f32 v133, v133, s65, v179
	v_pk_mul_f32 v[130:131], v[130:131], v[136:137]
	v_rcp_f32_e32 v134, v134
	v_rcp_f32_e32 v135, v135
	v_mov_b32_e32 v137, v167
	v_cvt_pk_fp8_f32 v137, v130, v131
	v_mov_b32_e32 v136, v167
	v_cvt_pk_fp8_f32 v136, v14, v15
	v_pk_fma_f32 v[14:15], v[132:133], v[16:17], v[16:17]
	v_pk_fma_f32 v[114:115], v[114:115], s[30:31], v[22:23] op_sel_hi:[1,0,1]
	v_pk_mul_f32 v[14:15], v[14:15], v[134:135]
	v_cvt_pk_fp8_f32 v136, v12, v13 op_sel:[0,0,1]
	v_cvt_pk_fp8_f32 v137, v14, v15 op_sel:[0,0,1]
	v_pk_fma_f32 v[14:15], v[122:123], s[30:31], v[30:31] op_sel_hi:[1,0,1]
	v_pk_fma_f32 v[12:13], v[124:125], s[30:31], v[32:33] op_sel_hi:[1,0,1]
	v_min_f32_e32 v14, 0x40e00000, v14
	v_min_f32_e32 v15, 0x40e00000, v15
	v_pk_mul_f32 v[16:17], v[14:15], s[34:35] op_sel_hi:[1,0]
	v_min_f32_e32 v12, 0x40e00000, v12
	v_exp_f32_e32 v16, v16
	v_exp_f32_e32 v17, v17
	v_min_f32_e32 v13, 0x40e00000, v13
	v_pk_fma_f32 v[124:125], v[126:127], s[30:31], v[26:27] op_sel_hi:[1,0,1]
	v_pk_mul_f32 v[126:127], v[12:13], s[34:35] op_sel_hi:[1,0]
	v_pk_add_f32 v[16:17], v[16:17], 1.0 op_sel_hi:[1,0]
	v_exp_f32_e32 v126, v126
	v_rcp_f32_e32 v16, v16
	v_rcp_f32_e32 v17, v17
	v_exp_f32_e32 v127, v127
	v_med3_f32 v124, v124, s65, v179
	v_med3_f32 v125, v125, s65, v179
	v_pk_fma_f32 v[14:15], v[124:125], v[14:15], v[14:15]
	v_pk_fma_f32 v[122:123], v[128:129], s[30:31], v[28:29] op_sel_hi:[1,0,1]
	v_pk_mul_f32 v[14:15], v[14:15], v[16:17]
	v_pk_add_f32 v[16:17], v[126:127], 1.0 op_sel_hi:[1,0]
	v_med3_f32 v122, v122, s65, v179
	v_rcp_f32_e32 v16, v16
	v_rcp_f32_e32 v17, v17
	v_med3_f32 v123, v123, s65, v179
	v_pk_fma_f32 v[12:13], v[122:123], v[12:13], v[12:13]
	v_min_f32_e32 v114, 0x40e00000, v114
	v_min_f32_e32 v115, 0x40e00000, v115
	v_pk_mul_f32 v[12:13], v[12:13], v[16:17]
	v_pk_fma_f32 v[16:17], v[116:117], s[30:31], v[24:25] op_sel_hi:[1,0,1]
	v_pk_fma_f32 v[116:117], v[120:121], s[30:31], v[20:21] op_sel_hi:[1,0,1]
	v_pk_mul_f32 v[120:121], v[114:115], s[34:35] op_sel_hi:[1,0]
	v_pk_fma_f32 v[118:119], v[118:119], s[30:31], v[18:19] op_sel_hi:[1,0,1]
	v_exp_f32_e32 v120, v120
	v_exp_f32_e32 v121, v121
	v_med3_f32 v118, v118, s65, v179
	v_med3_f32 v119, v119, s65, v179
	v_min_f32_e32 v16, 0x40e00000, v16
	v_min_f32_e32 v17, 0x40e00000, v17
	v_rcp_f32_e32 v146, v146
	v_rcp_f32_e32 v147, v147
	v_pk_add_f32 v[120:121], v[120:121], 1.0 op_sel_hi:[1,0]
	v_pk_fma_f32 v[114:115], v[118:119], v[114:115], v[114:115]
	v_pk_mul_f32 v[118:119], v[16:17], s[34:35] op_sel_hi:[1,0]
	v_rcp_f32_e32 v120, v120
	v_rcp_f32_e32 v121, v121
	v_exp_f32_e32 v118, v118
	v_exp_f32_e32 v119, v119
	s_lshr_b32 s39, s39, 1
	v_pk_mul_f32 v[10:11], v[10:11], v[146:147]
	s_lshl_b32 s41, s44, 7
	s_and_b32 s39, s39, 0x60
	v_cvt_pk_fp8_f32 v149, v10, v11 op_sel:[0,0,1]
	v_or_b32_e32 v10, 16, v6
	v_pk_mul_f32 v[114:115], v[114:115], v[120:121]
	v_pk_add_f32 v[118:119], v[118:119], 1.0 op_sel_hi:[1,0]
	v_mov_b32_e32 v120, v167
	s_or_b32 s41, s39, s41
	v_ashrrev_i32_e32 v11, 31, v10
	v_rcp_f32_e32 v118, v118
	v_rcp_f32_e32 v119, v119
	v_cvt_pk_fp8_f32 v120, v14, v15
	v_mov_b32_e32 v121, v167
	v_or_b32_e32 v4, s41, v8
	v_lshlrev_b64 v[10:11], 11, v[10:11]
	v_cvt_pk_fp8_f32 v121, v114, v115
	v_ashrrev_i32_e32 v5, 31, v4
	v_lshl_add_u64 v[10:11], s[16:17], 0, v[10:11]
	v_med3_f32 v116, v116, s65, v179
	v_med3_f32 v117, v117, s65, v179
	v_lshl_add_u64 v[10:11], v[10:11], 0, v[4:5]
	v_pk_fma_f32 v[14:15], v[116:117], v[16:17], v[16:17]
	global_store_dwordx2 v[10:11], v[136:137], off
	v_or_b32_e32 v10, 32, v6
	v_pk_mul_f32 v[14:15], v[14:15], v[118:119]
	v_cvt_pk_fp8_f32 v120, v12, v13 op_sel:[0,0,1]
	v_pk_fma_f32 v[12:13], v[106:107], s[30:31], v[30:31] op_sel_hi:[1,0,1]
	v_ashrrev_i32_e32 v11, 31, v10
	v_cvt_pk_fp8_f32 v121, v14, v15 op_sel:[0,0,1]
	v_min_f32_e32 v12, 0x40e00000, v12
	v_min_f32_e32 v13, 0x40e00000, v13
	v_lshlrev_b64 v[10:11], 11, v[10:11]
	v_pk_mul_f32 v[14:15], v[12:13], s[34:35] op_sel_hi:[1,0]
	v_lshl_add_u64 v[10:11], s[16:17], 0, v[10:11]
	v_exp_f32_e32 v14, v14
	v_exp_f32_e32 v15, v15
	v_lshl_add_u64 v[10:11], v[10:11], 0, v[4:5]
	global_store_dwordx2 v[10:11], v[120:121], off
	v_pk_fma_f32 v[10:11], v[108:109], s[30:31], v[32:33] op_sel_hi:[1,0,1]
	v_pk_add_f32 v[14:15], v[14:15], 1.0 op_sel_hi:[1,0]
	v_min_f32_e32 v10, 0x40e00000, v10
	v_min_f32_e32 v11, 0x40e00000, v11
	v_pk_mul_f32 v[108:109], v[10:11], s[34:35] op_sel_hi:[1,0]
	v_rcp_f32_e32 v14, v14
	v_rcp_f32_e32 v15, v15
	v_exp_f32_e32 v108, v108
	v_exp_f32_e32 v109, v109
	v_pk_fma_f32 v[106:107], v[110:111], s[30:31], v[26:27] op_sel_hi:[1,0,1]
	v_pk_fma_f32 v[16:17], v[112:113], s[30:31], v[28:29] op_sel_hi:[1,0,1]
	v_med3_f32 v106, v106, s65, v179
	v_med3_f32 v107, v107, s65, v179
	v_pk_fma_f32 v[12:13], v[106:107], v[12:13], v[12:13]
	v_med3_f32 v16, v16, s65, v179
	v_pk_mul_f32 v[12:13], v[12:13], v[14:15]
	v_pk_add_f32 v[14:15], v[108:109], 1.0 op_sel_hi:[1,0]
	v_med3_f32 v17, v17, s65, v179
	v_rcp_f32_e32 v14, v14
	v_rcp_f32_e32 v15, v15
	v_pk_fma_f32 v[10:11], v[16:17], v[10:11], v[10:11]
	v_pk_fma_f32 v[16:17], v[90:91], s[30:31], v[22:23] op_sel_hi:[1,0,1]
	v_pk_fma_f32 v[98:99], v[98:99], s[30:31], v[18:19] op_sel_hi:[1,0,1]
	v_min_f32_e32 v16, 0x40e00000, v16
	v_min_f32_e32 v17, 0x40e00000, v17
	v_pk_mul_f32 v[10:11], v[10:11], v[14:15]
	v_pk_fma_f32 v[14:15], v[92:93], s[30:31], v[24:25] op_sel_hi:[1,0,1]
	v_pk_mul_f32 v[92:93], v[16:17], s[34:35] op_sel_hi:[1,0]
	v_med3_f32 v98, v98, s65, v179
	v_exp_f32_e32 v92, v92
	v_exp_f32_e32 v93, v93
	v_med3_f32 v99, v99, s65, v179
	v_min_f32_e32 v14, 0x40e00000, v14
	v_min_f32_e32 v15, 0x40e00000, v15
	v_pk_add_f32 v[92:93], v[92:93], 1.0 op_sel_hi:[1,0]
	v_pk_fma_f32 v[16:17], v[98:99], v[16:17], v[16:17]
	v_pk_mul_f32 v[98:99], v[14:15], s[34:35] op_sel_hi:[1,0]
	v_rcp_f32_e32 v92, v92
	v_rcp_f32_e32 v93, v93
	v_exp_f32_e32 v98, v98
	v_exp_f32_e32 v99, v99
	v_ashrrev_i32_e32 v7, 31, v6
	v_pk_mul_f32 v[16:17], v[16:17], v[92:93]
	v_cvt_pk_fp8_f32 v148, v2, v3 op_sel:[0,0,1]
	v_pk_add_f32 v[92:93], v[98:99], 1.0 op_sel_hi:[1,0]
	v_lshlrev_b64 v[2:3], 11, v[6:7]
	v_or_b32_e32 v6, 48, v6
	v_rcp_f32_e32 v92, v92
	v_rcp_f32_e32 v93, v93
	v_mov_b32_e32 v98, v167
	v_mov_b32_e32 v99, v167
	v_ashrrev_i32_e32 v7, 31, v6
	v_pk_fma_f32 v[90:91], v[100:101], s[30:31], v[20:21] op_sel_hi:[1,0,1]
	v_cvt_pk_fp8_f32 v98, v12, v13
	v_cvt_pk_fp8_f32 v99, v16, v17
	v_med3_f32 v90, v90, s65, v179
	v_med3_f32 v91, v91, s65, v179
	v_lshlrev_b64 v[6:7], 11, v[6:7]
	v_lshl_add_u64 v[2:3], s[16:17], 0, v[2:3]
	v_pk_fma_f32 v[12:13], v[90:91], v[14:15], v[14:15]
	v_lshl_add_u64 v[6:7], s[16:17], 0, v[6:7]
	v_lshl_add_u64 v[2:3], v[2:3], 0, v[4:5]
	v_pk_mul_f32 v[12:13], v[12:13], v[92:93]
	v_lshl_add_u64 v[4:5], v[6:7], 0, v[4:5]
	v_pk_fma_f32 v[6:7], v[94:95], s[30:31], v[30:31] op_sel_hi:[1,0,1]
	v_cvt_pk_fp8_f32 v98, v10, v11 op_sel:[0,0,1]
	v_cvt_pk_fp8_f32 v99, v12, v13 op_sel:[0,0,1]
	v_min_f32_e32 v6, 0x40e00000, v6
	v_min_f32_e32 v7, 0x40e00000, v7
	v_pk_mul_f32 v[10:11], v[6:7], s[34:35] op_sel_hi:[1,0]
	global_store_dwordx2 v[4:5], v[98:99], off
	v_exp_f32_e32 v10, v10
	v_exp_f32_e32 v11, v11
	v_pk_fma_f32 v[4:5], v[96:97], s[30:31], v[32:33] op_sel_hi:[1,0,1]
	v_pk_fma_f32 v[14:15], v[102:103], s[30:31], v[26:27] op_sel_hi:[1,0,1]
	v_min_f32_e32 v4, 0x40e00000, v4
	v_min_f32_e32 v5, 0x40e00000, v5
	v_pk_add_f32 v[10:11], v[10:11], 1.0 op_sel_hi:[1,0]
	v_pk_mul_f32 v[16:17], v[4:5], s[34:35] op_sel_hi:[1,0]
	v_rcp_f32_e32 v10, v10
	v_rcp_f32_e32 v11, v11
	v_exp_f32_e32 v16, v16
	v_exp_f32_e32 v17, v17
	v_pk_fma_f32 v[12:13], v[104:105], s[30:31], v[28:29] op_sel_hi:[1,0,1]
	v_med3_f32 v14, v14, s65, v179
	v_med3_f32 v15, v15, s65, v179
	v_pk_fma_f32 v[6:7], v[14:15], v[6:7], v[6:7]
	v_med3_f32 v12, v12, s65, v179
	v_med3_f32 v13, v13, s65, v179
	v_pk_mul_f32 v[6:7], v[6:7], v[10:11]
	v_pk_add_f32 v[10:11], v[16:17], 1.0 op_sel_hi:[1,0]
	v_pk_fma_f32 v[4:5], v[12:13], v[4:5], v[4:5]
	v_pk_fma_f32 v[12:13], v[82:83], s[30:31], v[22:23] op_sel_hi:[1,0,1]
	v_rcp_f32_e32 v10, v10
	v_rcp_f32_e32 v11, v11
	v_min_f32_e32 v12, 0x40e00000, v12
	v_min_f32_e32 v13, 0x40e00000, v13
	v_pk_mul_f32 v[16:17], v[12:13], s[34:35] op_sel_hi:[1,0]
	v_pk_mul_f32 v[4:5], v[4:5], v[10:11]
	v_exp_f32_e32 v16, v16
	v_exp_f32_e32 v17, v17
	v_pk_fma_f32 v[10:11], v[84:85], s[30:31], v[24:25] op_sel_hi:[1,0,1]
	v_pk_fma_f32 v[82:83], v[86:87], s[30:31], v[18:19] op_sel_hi:[1,0,1]
	v_min_f32_e32 v10, 0x40e00000, v10
	v_med3_f32 v82, v82, s65, v179
	v_med3_f32 v83, v83, s65, v179
	v_min_f32_e32 v11, 0x40e00000, v11
	v_pk_add_f32 v[16:17], v[16:17], 1.0 op_sel_hi:[1,0]
	v_pk_fma_f32 v[12:13], v[82:83], v[12:13], v[12:13]
	v_pk_mul_f32 v[82:83], v[10:11], s[34:35] op_sel_hi:[1,0]
	v_rcp_f32_e32 v16, v16
	v_rcp_f32_e32 v17, v17
	v_exp_f32_e32 v82, v82
	v_exp_f32_e32 v83, v83
	v_pk_fma_f32 v[14:15], v[88:89], s[30:31], v[20:21] op_sel_hi:[1,0,1]
	v_pk_mul_f32 v[12:13], v[12:13], v[16:17]
	v_med3_f32 v14, v14, s65, v179
	v_pk_add_f32 v[16:17], v[82:83], 1.0 op_sel_hi:[1,0]
	v_mov_b32_e32 v83, v167
	v_rcp_f32_e32 v16, v16
	v_rcp_f32_e32 v17, v17
	v_mov_b32_e32 v82, v167
	v_cvt_pk_fp8_f32 v83, v12, v13
	v_med3_f32 v15, v15, s65, v179
	v_cvt_pk_fp8_f32 v82, v6, v7
	v_pk_fma_f32 v[6:7], v[14:15], v[10:11], v[10:11]
	s_mov_b32 s41, 0x40000
	v_pk_mul_f32 v[6:7], v[6:7], v[16:17]
	v_cvt_pk_fp8_f32 v82, v4, v5 op_sel:[0,0,1]
	v_cvt_pk_fp8_f32 v83, v6, v7 op_sel:[0,0,1]
	v_pk_fma_f32 v[6:7], v[74:75], s[30:31], v[30:31] op_sel_hi:[1,0,1]
	v_add_co_u32_e32 v4, vcc, s41, v2
	v_min_f32_e32 v6, 0x40e00000, v6
	v_min_f32_e32 v7, 0x40e00000, v7
	v_pk_mul_f32 v[10:11], v[6:7], s[34:35] op_sel_hi:[1,0]
	v_addc_co_u32_e32 v5, vcc, 0, v3, vcc
	v_exp_f32_e32 v10, v10
	v_exp_f32_e32 v11, v11
	global_store_dwordx2 v[4:5], v[82:83], off
	v_pk_fma_f32 v[4:5], v[76:77], s[30:31], v[32:33] op_sel_hi:[1,0,1]
	v_pk_fma_f32 v[14:15], v[78:79], s[30:31], v[26:27] op_sel_hi:[1,0,1]
	v_min_f32_e32 v4, 0x40e00000, v4
	v_min_f32_e32 v5, 0x40e00000, v5
	v_pk_add_f32 v[10:11], v[10:11], 1.0 op_sel_hi:[1,0]
	v_pk_mul_f32 v[16:17], v[4:5], s[34:35] op_sel_hi:[1,0]
	v_rcp_f32_e32 v10, v10
	v_rcp_f32_e32 v11, v11
	v_exp_f32_e32 v16, v16
	v_exp_f32_e32 v17, v17
	v_pk_fma_f32 v[12:13], v[80:81], s[30:31], v[28:29] op_sel_hi:[1,0,1]
	v_med3_f32 v14, v14, s65, v179
	v_med3_f32 v15, v15, s65, v179
	v_pk_fma_f32 v[6:7], v[14:15], v[6:7], v[6:7]
	v_med3_f32 v12, v12, s65, v179
	v_med3_f32 v13, v13, s65, v179
	v_pk_mul_f32 v[6:7], v[6:7], v[10:11]
	v_pk_add_f32 v[10:11], v[16:17], 1.0 op_sel_hi:[1,0]
	v_pk_fma_f32 v[4:5], v[12:13], v[4:5], v[4:5]
	v_pk_fma_f32 v[12:13], v[66:67], s[30:31], v[22:23] op_sel_hi:[1,0,1]
	v_rcp_f32_e32 v10, v10
	v_rcp_f32_e32 v11, v11
	v_min_f32_e32 v12, 0x40e00000, v12
	v_min_f32_e32 v13, 0x40e00000, v13
	v_pk_mul_f32 v[16:17], v[12:13], s[34:35] op_sel_hi:[1,0]
	v_pk_mul_f32 v[4:5], v[4:5], v[10:11]
	v_exp_f32_e32 v16, v16
	v_exp_f32_e32 v17, v17
	v_pk_fma_f32 v[10:11], v[68:69], s[30:31], v[24:25] op_sel_hi:[1,0,1]
	v_pk_fma_f32 v[66:67], v[70:71], s[30:31], v[18:19] op_sel_hi:[1,0,1]
	v_min_f32_e32 v10, 0x40e00000, v10
	v_med3_f32 v66, v66, s65, v179
	v_med3_f32 v67, v67, s65, v179
	v_min_f32_e32 v11, 0x40e00000, v11
	v_pk_add_f32 v[16:17], v[16:17], 1.0 op_sel_hi:[1,0]
	v_pk_fma_f32 v[12:13], v[66:67], v[12:13], v[12:13]
	v_pk_mul_f32 v[66:67], v[10:11], s[34:35] op_sel_hi:[1,0]
	v_rcp_f32_e32 v16, v16
	v_rcp_f32_e32 v17, v17
	v_exp_f32_e32 v66, v66
	v_exp_f32_e32 v67, v67
	v_pk_fma_f32 v[14:15], v[72:73], s[30:31], v[20:21] op_sel_hi:[1,0,1]
	v_pk_mul_f32 v[12:13], v[12:13], v[16:17]
	v_med3_f32 v14, v14, s65, v179
	v_pk_add_f32 v[16:17], v[66:67], 1.0 op_sel_hi:[1,0]
	v_mov_b32_e32 v67, v167
	v_rcp_f32_e32 v16, v16
	v_rcp_f32_e32 v17, v17
	v_mov_b32_e32 v66, v167
	v_cvt_pk_fp8_f32 v67, v12, v13
	v_med3_f32 v15, v15, s65, v179
	v_cvt_pk_fp8_f32 v66, v6, v7
	v_pk_fma_f32 v[6:7], v[14:15], v[10:11], v[10:11]
	s_mov_b32 s41, 0x48000
	v_pk_mul_f32 v[6:7], v[6:7], v[16:17]
	v_cvt_pk_fp8_f32 v66, v4, v5 op_sel:[0,0,1]
	v_cvt_pk_fp8_f32 v67, v6, v7 op_sel:[0,0,1]
	v_pk_fma_f32 v[6:7], v[58:59], s[30:31], v[30:31] op_sel_hi:[1,0,1]
	v_add_co_u32_e32 v4, vcc, s41, v2
	v_min_f32_e32 v6, 0x40e00000, v6
	v_min_f32_e32 v7, 0x40e00000, v7
	v_pk_mul_f32 v[10:11], v[6:7], s[34:35] op_sel_hi:[1,0]
	v_addc_co_u32_e32 v5, vcc, 0, v3, vcc
	v_exp_f32_e32 v10, v10
	v_exp_f32_e32 v11, v11
	global_store_dwordx2 v[4:5], v[66:67], off
	v_pk_fma_f32 v[4:5], v[60:61], s[30:31], v[32:33] op_sel_hi:[1,0,1]
	v_pk_fma_f32 v[14:15], v[62:63], s[30:31], v[26:27] op_sel_hi:[1,0,1]
	v_min_f32_e32 v4, 0x40e00000, v4
	v_min_f32_e32 v5, 0x40e00000, v5
	v_pk_add_f32 v[10:11], v[10:11], 1.0 op_sel_hi:[1,0]
	v_pk_mul_f32 v[16:17], v[4:5], s[34:35] op_sel_hi:[1,0]
	v_rcp_f32_e32 v10, v10
	v_rcp_f32_e32 v11, v11
	v_exp_f32_e32 v16, v16
	v_exp_f32_e32 v17, v17
	v_pk_fma_f32 v[12:13], v[64:65], s[30:31], v[28:29] op_sel_hi:[1,0,1]
	v_med3_f32 v14, v14, s65, v179
	v_med3_f32 v15, v15, s65, v179
	v_pk_fma_f32 v[6:7], v[14:15], v[6:7], v[6:7]
	v_med3_f32 v12, v12, s65, v179
	v_med3_f32 v13, v13, s65, v179
	v_pk_mul_f32 v[6:7], v[6:7], v[10:11]
	v_pk_add_f32 v[10:11], v[16:17], 1.0 op_sel_hi:[1,0]
	v_pk_fma_f32 v[4:5], v[12:13], v[4:5], v[4:5]
	v_pk_fma_f32 v[12:13], v[50:51], s[30:31], v[22:23] op_sel_hi:[1,0,1]
	v_rcp_f32_e32 v10, v10
	v_rcp_f32_e32 v11, v11
	v_min_f32_e32 v12, 0x40e00000, v12
	v_min_f32_e32 v13, 0x40e00000, v13
	v_pk_mul_f32 v[16:17], v[12:13], s[34:35] op_sel_hi:[1,0]
	v_pk_mul_f32 v[4:5], v[4:5], v[10:11]
	v_exp_f32_e32 v16, v16
	v_exp_f32_e32 v17, v17
	v_pk_fma_f32 v[10:11], v[52:53], s[30:31], v[24:25] op_sel_hi:[1,0,1]
	v_pk_fma_f32 v[50:51], v[54:55], s[30:31], v[18:19] op_sel_hi:[1,0,1]
	v_min_f32_e32 v10, 0x40e00000, v10
	v_med3_f32 v50, v50, s65, v179
	v_med3_f32 v51, v51, s65, v179
	v_min_f32_e32 v11, 0x40e00000, v11
	v_pk_add_f32 v[16:17], v[16:17], 1.0 op_sel_hi:[1,0]
	v_pk_fma_f32 v[12:13], v[50:51], v[12:13], v[12:13]
	v_pk_mul_f32 v[50:51], v[10:11], s[34:35] op_sel_hi:[1,0]
	v_rcp_f32_e32 v16, v16
	v_rcp_f32_e32 v17, v17
	v_exp_f32_e32 v50, v50
	v_exp_f32_e32 v51, v51
	v_pk_fma_f32 v[14:15], v[56:57], s[30:31], v[20:21] op_sel_hi:[1,0,1]
	v_pk_mul_f32 v[12:13], v[12:13], v[16:17]
	v_med3_f32 v14, v14, s65, v179
	v_pk_add_f32 v[16:17], v[50:51], 1.0 op_sel_hi:[1,0]
	v_mov_b32_e32 v51, v167
	v_rcp_f32_e32 v16, v16
	v_rcp_f32_e32 v17, v17
	v_mov_b32_e32 v50, v167
	v_cvt_pk_fp8_f32 v51, v12, v13
	v_med3_f32 v15, v15, s65, v179
	v_cvt_pk_fp8_f32 v50, v6, v7
	v_pk_fma_f32 v[6:7], v[14:15], v[10:11], v[10:11]
	s_mov_b32 s41, 0x50000
	v_pk_mul_f32 v[6:7], v[6:7], v[16:17]
	v_cvt_pk_fp8_f32 v50, v4, v5 op_sel:[0,0,1]
	v_cvt_pk_fp8_f32 v51, v6, v7 op_sel:[0,0,1]
	v_pk_fma_f32 v[6:7], v[42:43], s[30:31], v[30:31] op_sel_hi:[1,0,1]
	v_add_co_u32_e32 v4, vcc, s41, v2
	v_min_f32_e32 v6, 0x40e00000, v6
	v_min_f32_e32 v7, 0x40e00000, v7
	v_pk_mul_f32 v[10:11], v[6:7], s[34:35] op_sel_hi:[1,0]
	v_addc_co_u32_e32 v5, vcc, 0, v3, vcc
	v_exp_f32_e32 v10, v10
	v_exp_f32_e32 v11, v11
	global_store_dwordx2 v[4:5], v[50:51], off
	v_pk_fma_f32 v[4:5], v[44:45], s[30:31], v[32:33] op_sel_hi:[1,0,1]
	v_pk_fma_f32 v[14:15], v[46:47], s[30:31], v[26:27] op_sel_hi:[1,0,1]
	v_min_f32_e32 v4, 0x40e00000, v4
	v_min_f32_e32 v5, 0x40e00000, v5
	v_pk_add_f32 v[10:11], v[10:11], 1.0 op_sel_hi:[1,0]
	v_pk_mul_f32 v[16:17], v[4:5], s[34:35] op_sel_hi:[1,0]
	v_rcp_f32_e32 v10, v10
	v_rcp_f32_e32 v11, v11
	v_exp_f32_e32 v16, v16
	v_exp_f32_e32 v17, v17
	v_pk_fma_f32 v[12:13], v[48:49], s[30:31], v[28:29] op_sel_hi:[1,0,1]
	v_med3_f32 v14, v14, s65, v179
	v_med3_f32 v15, v15, s65, v179
	v_pk_fma_f32 v[6:7], v[14:15], v[6:7], v[6:7]
	v_med3_f32 v12, v12, s65, v179
	v_med3_f32 v13, v13, s65, v179
	v_pk_mul_f32 v[6:7], v[6:7], v[10:11]
	v_pk_add_f32 v[10:11], v[16:17], 1.0 op_sel_hi:[1,0]
	v_pk_fma_f32 v[4:5], v[12:13], v[4:5], v[4:5]
	v_pk_fma_f32 v[12:13], v[34:35], s[30:31], v[22:23] op_sel_hi:[1,0,1]
	v_rcp_f32_e32 v10, v10
	v_rcp_f32_e32 v11, v11
	v_min_f32_e32 v12, 0x40e00000, v12
	v_min_f32_e32 v13, 0x40e00000, v13
	v_pk_mul_f32 v[16:17], v[12:13], s[34:35] op_sel_hi:[1,0]
	v_pk_mul_f32 v[4:5], v[4:5], v[10:11]
	v_exp_f32_e32 v16, v16
	v_exp_f32_e32 v17, v17
	v_pk_fma_f32 v[10:11], v[36:37], s[30:31], v[24:25] op_sel_hi:[1,0,1]
	v_pk_fma_f32 v[18:19], v[38:39], s[30:31], v[18:19] op_sel_hi:[1,0,1]
	v_min_f32_e32 v10, 0x40e00000, v10
	v_med3_f32 v18, v18, s65, v179
	v_med3_f32 v19, v19, s65, v179
	v_min_f32_e32 v11, 0x40e00000, v11
	v_pk_add_f32 v[16:17], v[16:17], 1.0 op_sel_hi:[1,0]
	v_pk_fma_f32 v[12:13], v[18:19], v[12:13], v[12:13]
	v_pk_mul_f32 v[18:19], v[10:11], s[34:35] op_sel_hi:[1,0]
	v_rcp_f32_e32 v16, v16
	v_rcp_f32_e32 v17, v17
	v_exp_f32_e32 v18, v18
	v_exp_f32_e32 v19, v19
	v_pk_fma_f32 v[14:15], v[40:41], s[30:31], v[20:21] op_sel_hi:[1,0,1]
	v_pk_mul_f32 v[12:13], v[12:13], v[16:17]
	v_med3_f32 v14, v14, s65, v179
	v_pk_add_f32 v[16:17], v[18:19], 1.0 op_sel_hi:[1,0]
	v_mov_b32_e32 v18, v167
	v_rcp_f32_e32 v16, v16
	v_rcp_f32_e32 v17, v17
	v_mov_b32_e32 v19, v167
	v_cvt_pk_fp8_f32 v18, v6, v7
	v_cvt_pk_fp8_f32 v19, v12, v13
	v_med3_f32 v15, v15, s65, v179
	v_pk_fma_f32 v[6:7], v[14:15], v[10:11], v[10:11]
	v_cvt_pk_fp8_f32 v18, v4, v5 op_sel:[0,0,1]
	v_pk_mul_f32 v[6:7], v[6:7], v[16:17]
	global_store_dwordx2 v[2:3], v[148:149], off
	v_cvt_pk_fp8_f32 v19, v6, v7 op_sel:[0,0,1]
	v_add_co_u32_e32 v2, vcc, 0x58000, v2
	s_mov_b64 s[44:45], -1
	s_nop 0
	v_addc_co_u32_e32 v3, vcc, 0, v3, vcc
	s_and_b64 vcc, s[42:43], exec
	global_store_dwordx2 v[2:3], v[18:19], off
	s_cbranch_vccz .LBB0_1434
	s_ashr_i32 s41, s40, 31
	s_lshl_b64 s[42:43], s[40:41], 14
	s_add_u32 s41, s88, s42
	s_addc_u32 s44, s89, s43
	s_lshl_b32 s42, s38, 7
	s_ashr_i32 s43, s42, 31
	s_lshl_b64 s[42:43], s[42:43], 2
	s_add_u32 s41, s41, s42
	s_addc_u32 s43, s44, s43
	s_lshl_b32 s39, s39, 2
	s_add_u32 s42, s41, s39
	s_addc_u32 s43, s43, 0
	v_lshlrev_b32_e32 v166, 2, v8
	v_lshl_add_u64 v[2:3], s[42:43], 0, v[166:167]
	v_lshl_add_u64 v[4:5], v[2:3], 0, 16
	s_mov_b64 s[44:45], 0
	global_load_dwordx4 v[30:33], v[2:3], off
	global_load_dwordx4 v[22:25], v[4:5], off
	v_lshl_add_u64 v[4:5], v[2:3], 0, s[12:13]
	global_load_dwordx4 v[26:29], v[4:5], off
	v_lshl_add_u64 v[2:3], v[2:3], 0, s[14:15]
	global_load_dwordx4 v[18:21], v[2:3], off
	s_branch .LBB0_1434

.LBB0_1547:
	ds_read_b128 v[10:13], v183
	ds_read_b128 v[14:17], v183 offset:1024
	ds_read_b128 v[174:177], v183 offset:2048
	ds_read_b128 v[178:181], v183 offset:3072
	s_add_u32 s46, s44, 0xfffc0080
	s_addc_u32 s47, s45, -1
	s_cmp_eq_u32 s80, 12
	s_cselect_b32 s49, s27, s47
	s_cselect_b32 s48, s31, s46
	s_cselect_b32 s47, s25, s79
	s_cselect_b32 s46, s39, s78
	s_mov_b32 m0, s68
	v_lshl_add_u64 v[2:3], s[44:45], 0, v[170:171]
	ds_read_b128 v[188:191], v184
	ds_read_b128 v[192:195], v184 offset:1024
	ds_read_b128 v[196:199], v184 offset:2048
	ds_read_b128 v[200:203], v184 offset:3072
	ds_read_b128 v[204:207], v184 offset:4096
	ds_read_b128 v[208:211], v184 offset:5120
	ds_read_b128 v[212:215], v184 offset:6144
	ds_read_b128 v[216:219], v184 offset:7168
	global_load_lds_dwordx4 v[2:3], off
	v_lshl_add_u64 v[2:3], s[44:45], 0, v[172:173]
	s_mov_b32 m0, s69
	s_nop 0
	global_load_lds_dwordx4 v[2:3], off
	ds_read_b128 v[220:223], v185
	ds_read_b128 v[224:227], v185 offset:1024
	ds_read_b128 v[228:231], v185 offset:2048
	ds_read_b128 v[232:235], v185 offset:3072
	s_waitcnt vmcnt(8) lgkmcnt(0)
	s_barrier
	s_setprio 1
	v_mfma_scale_f32_16x16x128_f8f6f4 v[150:153], v[10:17], v[188:195], v[150:153], v1, v1 op_sel_hi:[0,0,0]
	v_mfma_scale_f32_16x16x128_f8f6f4 v[146:149], v[174:181], v[188:195], v[146:149], v1, v1 op_sel_hi:[0,0,0]
	v_mfma_scale_f32_16x16x128_f8f6f4 v[134:137], v[10:17], v[196:203], v[134:137], v1, v1 op_sel_hi:[0,0,0]
	v_mfma_scale_f32_16x16x128_f8f6f4 v[130:133], v[174:181], v[196:203], v[130:133], v1, v1 op_sel_hi:[0,0,0]
	v_mfma_scale_f32_16x16x128_f8f6f4 v[118:121], v[10:17], v[204:211], v[118:121], v1, v1 op_sel_hi:[0,0,0]
	v_mfma_scale_f32_16x16x128_f8f6f4 v[114:117], v[174:181], v[204:211], v[114:117], v1, v1 op_sel_hi:[0,0,0]
	v_mfma_scale_f32_16x16x128_f8f6f4 v[86:89], v[10:17], v[212:219], v[86:89], v1, v1 op_sel_hi:[0,0,0]
	v_mfma_scale_f32_16x16x128_f8f6f4 v[82:85], v[174:181], v[212:219], v[82:85], v1, v1 op_sel_hi:[0,0,0]
	v_mfma_scale_f32_16x16x128_f8f6f4 v[158:161], v[220:227], v[188:195], v[158:161], v1, v1 op_sel_hi:[0,0,0]
	v_mfma_scale_f32_16x16x128_f8f6f4 v[154:157], v[228:235], v[188:195], v[154:157], v1, v1 op_sel_hi:[0,0,0]
	v_mfma_scale_f32_16x16x128_f8f6f4 v[142:145], v[220:227], v[196:203], v[142:145], v1, v1 op_sel_hi:[0,0,0]
	v_mfma_scale_f32_16x16x128_f8f6f4 v[138:141], v[228:235], v[196:203], v[138:141], v1, v1 op_sel_hi:[0,0,0]
	v_mfma_scale_f32_16x16x128_f8f6f4 v[126:129], v[220:227], v[204:211], v[126:129], v1, v1 op_sel_hi:[0,0,0]
	v_mfma_scale_f32_16x16x128_f8f6f4 v[122:125], v[228:235], v[204:211], v[122:125], v1, v1 op_sel_hi:[0,0,0]
	v_mfma_scale_f32_16x16x128_f8f6f4 v[94:97], v[220:227], v[212:219], v[94:97], v1, v1 op_sel_hi:[0,0,0]
	v_mfma_scale_f32_16x16x128_f8f6f4 v[90:93], v[228:235], v[212:219], v[90:93], v1, v1 op_sel_hi:[0,0,0]
	s_setprio 0
	s_barrier
	ds_read_b128 v[188:191], v184 offset:16384
	ds_read_b128 v[192:195], v184 offset:17408
	ds_read_b128 v[196:199], v184 offset:18432
	ds_read_b128 v[200:203], v184 offset:19456
	ds_read_b128 v[204:207], v184 offset:20480
	ds_read_b128 v[208:211], v184 offset:21504
	ds_read_b128 v[212:215], v184 offset:22528
	ds_read_b128 v[216:219], v184 offset:23552
	s_mov_b32 m0, s70
	v_lshl_add_u64 v[6:7], s[46:47], 0, v[164:165]
	global_load_lds_dwordx4 v[6:7], off
	v_lshl_add_u64 v[8:9], s[46:47], 0, v[168:169]
	s_mov_b32 m0, s71
	s_nop 0
	global_load_lds_dwordx4 v[8:9], off
	s_mov_b32 m0, s54
	v_lshl_add_u64 v[2:3], s[48:49], 0, v[162:163]
	global_load_lds_dwordx4 v[2:3], off
	v_lshl_add_u64 v[4:5], s[48:49], 0, v[166:167]
	s_mov_b32 m0, s55
	s_nop 0
	global_load_lds_dwordx4 v[4:5], off
	s_add_u32 s82, s46, 0x40000
	s_addc_u32 s83, s47, 0
	s_mov_b32 m0, s72
	v_lshl_add_u64 v[236:237], s[82:83], 0, v[164:165]
	global_load_lds_dwordx4 v[236:237], off
	v_lshl_add_u64 v[236:237], s[82:83], 0, v[168:169]
	s_mov_b32 m0, s73
	s_nop 0
	global_load_lds_dwordx4 v[236:237], off
	s_waitcnt vmcnt(8) lgkmcnt(0)
	s_barrier
	s_setprio 1
	v_mfma_scale_f32_16x16x128_f8f6f4 v[110:113], v[10:17], v[188:195], v[110:113], v1, v1 op_sel_hi:[0,0,0]
	v_mfma_scale_f32_16x16x128_f8f6f4 v[102:105], v[174:181], v[188:195], v[102:105], v1, v1 op_sel_hi:[0,0,0]
	v_mfma_scale_f32_16x16x128_f8f6f4 v[78:81], v[10:17], v[196:203], v[78:81], v1, v1 op_sel_hi:[0,0,0]
	v_mfma_scale_f32_16x16x128_f8f6f4 v[70:73], v[174:181], v[196:203], v[70:73], v1, v1 op_sel_hi:[0,0,0]
	v_mfma_scale_f32_16x16x128_f8f6f4 v[62:65], v[10:17], v[204:211], v[62:65], v1, v1 op_sel_hi:[0,0,0]
	v_mfma_scale_f32_16x16x128_f8f6f4 v[54:57], v[174:181], v[204:211], v[54:57], v1, v1 op_sel_hi:[0,0,0]
	v_mfma_scale_f32_16x16x128_f8f6f4 v[46:49], v[10:17], v[212:219], v[46:49], v1, v1 op_sel_hi:[0,0,0]
	v_mfma_scale_f32_16x16x128_f8f6f4 v[42:45], v[174:181], v[212:219], v[42:45], v1, v1 op_sel_hi:[0,0,0]
	v_mfma_scale_f32_16x16x128_f8f6f4 v[106:109], v[220:227], v[188:195], v[106:109], v1, v1 op_sel_hi:[0,0,0]
	v_mfma_scale_f32_16x16x128_f8f6f4 v[98:101], v[228:235], v[188:195], v[98:101], v1, v1 op_sel_hi:[0,0,0]
	v_mfma_scale_f32_16x16x128_f8f6f4 v[74:77], v[220:227], v[196:203], v[74:77], v1, v1 op_sel_hi:[0,0,0]
	v_mfma_scale_f32_16x16x128_f8f6f4 v[66:69], v[228:235], v[196:203], v[66:69], v1, v1 op_sel_hi:[0,0,0]
	v_mfma_scale_f32_16x16x128_f8f6f4 v[58:61], v[220:227], v[204:211], v[58:61], v1, v1 op_sel_hi:[0,0,0]
	v_mfma_scale_f32_16x16x128_f8f6f4 v[50:53], v[228:235], v[204:211], v[50:53], v1, v1 op_sel_hi:[0,0,0]
	v_mfma_scale_f32_16x16x128_f8f6f4 v[38:41], v[220:227], v[212:219], v[38:41], v1, v1 op_sel_hi:[0,0,0]
	v_mfma_scale_f32_16x16x128_f8f6f4 v[34:37], v[228:235], v[212:219], v[34:37], v1, v1 op_sel_hi:[0,0,0]
	s_setprio 0
	s_barrier
	ds_read_b128 v[10:13], v186
	ds_read_b128 v[14:17], v186 offset:1024
	ds_read_b128 v[174:177], v186 offset:2048
	ds_read_b128 v[178:181], v186 offset:3072
	s_add_u32 s48, s48, 0x40000
	s_addc_u32 s49, s49, 0
	s_mov_b32 m0, s56
	v_lshl_add_u64 v[220:221], s[48:49], 0, v[162:163]
	ds_read_b128 v[188:191], v184 offset:32768
	ds_read_b128 v[192:195], v184 offset:33792
	ds_read_b128 v[196:199], v184 offset:34816
	ds_read_b128 v[200:203], v184 offset:35840
	ds_read_b128 v[204:207], v184 offset:36864
	ds_read_b128 v[208:211], v184 offset:37888
	ds_read_b128 v[212:215], v184 offset:38912
	ds_read_b128 v[216:219], v184 offset:39936
	global_load_lds_dwordx4 v[220:221], off
	v_lshl_add_u64 v[220:221], s[48:49], 0, v[166:167]
	s_mov_b32 m0, s57
	s_nop 0
	global_load_lds_dwordx4 v[220:221], off
	ds_read_b128 v[220:223], v187
	ds_read_b128 v[224:227], v187 offset:1024
	ds_read_b128 v[228:231], v187 offset:2048
	ds_read_b128 v[232:235], v187 offset:3072
	s_waitcnt vmcnt(8) lgkmcnt(0)
	s_barrier
	s_setprio 1
	v_mfma_scale_f32_16x16x128_f8f6f4 v[150:153], v[10:17], v[188:195], v[150:153], v1, v1 op_sel_hi:[0,0,0]
	v_mfma_scale_f32_16x16x128_f8f6f4 v[146:149], v[174:181], v[188:195], v[146:149], v1, v1 op_sel_hi:[0,0,0]
	v_mfma_scale_f32_16x16x128_f8f6f4 v[134:137], v[10:17], v[196:203], v[134:137], v1, v1 op_sel_hi:[0,0,0]
	v_mfma_scale_f32_16x16x128_f8f6f4 v[130:133], v[174:181], v[196:203], v[130:133], v1, v1 op_sel_hi:[0,0,0]
	v_mfma_scale_f32_16x16x128_f8f6f4 v[118:121], v[10:17], v[204:211], v[118:121], v1, v1 op_sel_hi:[0,0,0]
	v_mfma_scale_f32_16x16x128_f8f6f4 v[114:117], v[174:181], v[204:211], v[114:117], v1, v1 op_sel_hi:[0,0,0]
	v_mfma_scale_f32_16x16x128_f8f6f4 v[86:89], v[10:17], v[212:219], v[86:89], v1, v1 op_sel_hi:[0,0,0]
	v_mfma_scale_f32_16x16x128_f8f6f4 v[82:85], v[174:181], v[212:219], v[82:85], v1, v1 op_sel_hi:[0,0,0]
	v_mfma_scale_f32_16x16x128_f8f6f4 v[158:161], v[220:227], v[188:195], v[158:161], v1, v1 op_sel_hi:[0,0,0]
	v_mfma_scale_f32_16x16x128_f8f6f4 v[154:157], v[228:235], v[188:195], v[154:157], v1, v1 op_sel_hi:[0,0,0]
	v_mfma_scale_f32_16x16x128_f8f6f4 v[142:145], v[220:227], v[196:203], v[142:145], v1, v1 op_sel_hi:[0,0,0]
	v_mfma_scale_f32_16x16x128_f8f6f4 v[138:141], v[228:235], v[196:203], v[138:141], v1, v1 op_sel_hi:[0,0,0]
	v_mfma_scale_f32_16x16x128_f8f6f4 v[126:129], v[220:227], v[204:211], v[126:129], v1, v1 op_sel_hi:[0,0,0]
	v_mfma_scale_f32_16x16x128_f8f6f4 v[122:125], v[228:235], v[204:211], v[122:125], v1, v1 op_sel_hi:[0,0,0]
	v_mfma_scale_f32_16x16x128_f8f6f4 v[94:97], v[220:227], v[212:219], v[94:97], v1, v1 op_sel_hi:[0,0,0]
	v_mfma_scale_f32_16x16x128_f8f6f4 v[90:93], v[228:235], v[212:219], v[90:93], v1, v1 op_sel_hi:[0,0,0]
	s_setprio 0
	s_barrier
	ds_read_b128 v[188:191], v184 offset:49152
	ds_read_b128 v[192:195], v184 offset:50176
	ds_read_b128 v[196:199], v184 offset:51200
	ds_read_b128 v[200:203], v184 offset:52224
	ds_read_b128 v[204:207], v184 offset:53248
	ds_read_b128 v[208:211], v184 offset:54272
	ds_read_b128 v[212:215], v184 offset:55296
	ds_read_b128 v[216:219], v184 offset:56320
	s_mov_b32 m0, s74
	v_lshl_add_u64 v[6:7], v[6:7], 0, s[10:11]
	global_load_lds_dwordx4 v[6:7], off
	v_lshl_add_u64 v[6:7], v[8:9], 0, s[10:11]
	s_mov_b32 m0, s75
	s_nop 0
	global_load_lds_dwordx4 v[6:7], off
	s_mov_b32 m0, s59
	v_lshl_add_u64 v[2:3], v[2:3], 0, s[10:11]
	global_load_lds_dwordx4 v[2:3], off
	v_lshl_add_u64 v[2:3], v[4:5], 0, s[10:11]
	s_mov_b32 m0, s60
	s_nop 0
	global_load_lds_dwordx4 v[2:3], off
	s_add_u32 s46, s46, 0x40080
	s_addc_u32 s47, s47, 0
	s_mov_b32 m0, s76
	v_lshl_add_u64 v[2:3], s[46:47], 0, v[164:165]
	global_load_lds_dwordx4 v[2:3], off
	v_lshl_add_u64 v[2:3], s[46:47], 0, v[168:169]
	s_mov_b32 m0, s77
	s_nop 0
	global_load_lds_dwordx4 v[2:3], off
	s_waitcnt vmcnt(8) lgkmcnt(0)
	s_barrier
	s_setprio 1
	v_mfma_scale_f32_16x16x128_f8f6f4 v[110:113], v[10:17], v[188:195], v[110:113], v1, v1 op_sel_hi:[0,0,0]
	v_mfma_scale_f32_16x16x128_f8f6f4 v[102:105], v[174:181], v[188:195], v[102:105], v1, v1 op_sel_hi:[0,0,0]
	v_mfma_scale_f32_16x16x128_f8f6f4 v[78:81], v[10:17], v[196:203], v[78:81], v1, v1 op_sel_hi:[0,0,0]
	v_mfma_scale_f32_16x16x128_f8f6f4 v[70:73], v[174:181], v[196:203], v[70:73], v1, v1 op_sel_hi:[0,0,0]
	v_mfma_scale_f32_16x16x128_f8f6f4 v[62:65], v[10:17], v[204:211], v[62:65], v1, v1 op_sel_hi:[0,0,0]
	v_mfma_scale_f32_16x16x128_f8f6f4 v[54:57], v[174:181], v[204:211], v[54:57], v1, v1 op_sel_hi:[0,0,0]
	v_mfma_scale_f32_16x16x128_f8f6f4 v[46:49], v[10:17], v[212:219], v[46:49], v1, v1 op_sel_hi:[0,0,0]
	v_mfma_scale_f32_16x16x128_f8f6f4 v[42:45], v[174:181], v[212:219], v[42:45], v1, v1 op_sel_hi:[0,0,0]
	v_mfma_scale_f32_16x16x128_f8f6f4 v[106:109], v[220:227], v[188:195], v[106:109], v1, v1 op_sel_hi:[0,0,0]
	v_mfma_scale_f32_16x16x128_f8f6f4 v[98:101], v[228:235], v[188:195], v[98:101], v1, v1 op_sel_hi:[0,0,0]
	v_mfma_scale_f32_16x16x128_f8f6f4 v[74:77], v[220:227], v[196:203], v[74:77], v1, v1 op_sel_hi:[0,0,0]
	v_mfma_scale_f32_16x16x128_f8f6f4 v[66:69], v[228:235], v[196:203], v[66:69], v1, v1 op_sel_hi:[0,0,0]
	v_mfma_scale_f32_16x16x128_f8f6f4 v[58:61], v[220:227], v[204:211], v[58:61], v1, v1 op_sel_hi:[0,0,0]
	v_mfma_scale_f32_16x16x128_f8f6f4 v[50:53], v[228:235], v[204:211], v[50:53], v1, v1 op_sel_hi:[0,0,0]
	v_mfma_scale_f32_16x16x128_f8f6f4 v[38:41], v[220:227], v[212:219], v[38:41], v1, v1 op_sel_hi:[0,0,0]
	v_mfma_scale_f32_16x16x128_f8f6f4 v[34:37], v[228:235], v[212:219], v[34:37], v1, v1 op_sel_hi:[0,0,0]
	s_setprio 0
	s_add_i32 s80, s80, 2
	s_add_u32 s44, s44, 0x100
	s_addc_u32 s45, s45, 0
	s_add_u32 s78, s78, 0x100
	s_addc_u32 s79, s79, 0
	s_cmp_gt_u32 s80, 13
	s_barrier
	s_cbranch_scc0 .LBB0_1547
	v_mov_b32_e32 v2, v0
	s_nop 15
	s_nop 15
	s_lshl_b32 s27, s40, 8
	v_readfirstlane_b32 s25, v2
	s_ashr_i32 s31, s25, 2
	s_andn2_b32 s31, s31, 63
	s_add_i32 s31, s31, s27
	s_lshr_b32 s25, s25, 1
	v_and_or_b32 v10, v2, 15, s31
	s_and_b32 s25, s25, 0x60
	v_lshrrev_b32_e32 v2, 1, v2
	s_lshl_b32 s27, s38, 8
	v_and_b32_e32 v4, 24, v2
	s_or_b32 s27, s25, s27
	v_or_b32_e32 v2, s27, v4
	v_ashrrev_i32_e32 v11, 31, v10
	v_ashrrev_i32_e32 v3, 31, v2
	v_lshlrev_b64 v[6:7], 12, v[10:11]
	v_lshl_add_u64 v[6:7], s[8:9], 0, v[6:7]
	v_lshlrev_b64 v[12:13], 1, v[2:3]
	s_waitcnt vmcnt(6)
	v_lshl_add_u64 v[2:3], v[6:7], 0, v[12:13]
	v_pk_fma_f32 v[6:7], v[150:151], s[18:19], v[22:23] op_sel_hi:[1,0,1]
	v_pk_fma_f32 v[8:9], v[152:153], s[18:19], v[24:25] op_sel_hi:[1,0,1]
	v_cvt_pk_bf16_f32 v6, v6, v7
	v_pk_fma_f32 v[14:15], v[148:149], s[18:19], v[20:21] op_sel_hi:[1,0,1]
	v_cvt_pk_bf16_f32 v7, v8, v9
	v_pk_fma_f32 v[16:17], v[146:147], s[18:19], v[18:19] op_sel_hi:[1,0,1]
	v_pk_fma_f32 v[130:131], v[130:131], s[18:19], v[18:19] op_sel_hi:[1,0,1]
	v_cvt_pk_bf16_f32 v8, v16, v17
	v_cvt_pk_bf16_f32 v9, v14, v15
	global_store_dwordx4 v[2:3], v[6:9], off
	v_pk_fma_f32 v[14:15], v[156:157], s[18:19], v[28:29] op_sel_hi:[1,0,1]
	v_pk_fma_f32 v[16:17], v[154:155], s[18:19], v[26:27] op_sel_hi:[1,0,1]
	v_pk_fma_f32 v[6:7], v[158:159], s[18:19], v[30:31] op_sel_hi:[1,0,1]
	v_pk_fma_f32 v[8:9], v[160:161], s[18:19], v[32:33] op_sel_hi:[1,0,1]
	v_cvt_pk_bf16_f32 v6, v6, v7
	v_pk_fma_f32 v[114:115], v[114:115], s[18:19], v[18:19] op_sel_hi:[1,0,1]
	v_cvt_pk_bf16_f32 v7, v8, v9
	v_cvt_pk_bf16_f32 v8, v16, v17
	v_cvt_pk_bf16_f32 v9, v14, v15
	global_store_dwordx4 v[2:3], v[6:9], off offset:256
	v_pk_fma_f32 v[16:17], v[132:133], s[18:19], v[20:21] op_sel_hi:[1,0,1]
	s_mov_b32 s27, 0x80000
	v_or_b32_e32 v6, 16, v10
	v_ashrrev_i32_e32 v7, 31, v6
	v_lshlrev_b64 v[6:7], 12, v[6:7]
	v_lshl_add_u64 v[6:7], s[8:9], 0, v[6:7]
	v_lshl_add_u64 v[14:15], v[6:7], 0, v[12:13]
	v_pk_fma_f32 v[6:7], v[134:135], s[18:19], v[22:23] op_sel_hi:[1,0,1]
	v_pk_fma_f32 v[8:9], v[136:137], s[18:19], v[24:25] op_sel_hi:[1,0,1]
	v_cvt_pk_bf16_f32 v6, v6, v7
	s_mov_b64 s[38:39], 0x80000
	v_cvt_pk_bf16_f32 v7, v8, v9
	v_cvt_pk_bf16_f32 v8, v130, v131
	v_cvt_pk_bf16_f32 v9, v16, v17
	global_store_dwordx4 v[14:15], v[6:9], off
	v_pk_fma_f32 v[16:17], v[140:141], s[18:19], v[28:29] op_sel_hi:[1,0,1]
	v_pk_fma_f32 v[130:131], v[138:139], s[18:19], v[26:27] op_sel_hi:[1,0,1]
	v_pk_fma_f32 v[6:7], v[142:143], s[18:19], v[30:31] op_sel_hi:[1,0,1]
	v_pk_fma_f32 v[8:9], v[144:145], s[18:19], v[32:33] op_sel_hi:[1,0,1]
	v_cvt_pk_bf16_f32 v6, v6, v7
	v_readlane_b32 s68, v254, 0
	v_cvt_pk_bf16_f32 v7, v8, v9
	v_cvt_pk_bf16_f32 v8, v130, v131
	v_cvt_pk_bf16_f32 v9, v16, v17
	global_store_dwordx4 v[14:15], v[6:9], off offset:256
	v_pk_fma_f32 v[16:17], v[116:117], s[18:19], v[20:21] op_sel_hi:[1,0,1]
	v_readlane_b32 s69, v254, 1
	v_or_b32_e32 v6, 32, v10
	v_ashrrev_i32_e32 v7, 31, v6
	v_lshlrev_b64 v[6:7], 12, v[6:7]
	v_lshl_add_u64 v[6:7], s[8:9], 0, v[6:7]
	v_lshl_add_u64 v[14:15], v[6:7], 0, v[12:13]
	v_pk_fma_f32 v[6:7], v[118:119], s[18:19], v[22:23] op_sel_hi:[1,0,1]
	v_pk_fma_f32 v[8:9], v[120:121], s[18:19], v[24:25] op_sel_hi:[1,0,1]
	v_cvt_pk_bf16_f32 v6, v6, v7
	v_readlane_b32 s70, v254, 2
	v_cvt_pk_bf16_f32 v7, v8, v9
	v_cvt_pk_bf16_f32 v8, v114, v115
	v_cvt_pk_bf16_f32 v9, v16, v17
	global_store_dwordx4 v[14:15], v[6:9], off
	v_pk_fma_f32 v[16:17], v[124:125], s[18:19], v[28:29] op_sel_hi:[1,0,1]
	v_pk_fma_f32 v[114:115], v[122:123], s[18:19], v[26:27] op_sel_hi:[1,0,1]
	v_pk_fma_f32 v[6:7], v[126:127], s[18:19], v[30:31] op_sel_hi:[1,0,1]
	v_pk_fma_f32 v[8:9], v[128:129], s[18:19], v[32:33] op_sel_hi:[1,0,1]
	v_cvt_pk_bf16_f32 v6, v6, v7
	v_readlane_b32 s71, v254, 3
	v_cvt_pk_bf16_f32 v7, v8, v9
	v_cvt_pk_bf16_f32 v8, v114, v115
	v_cvt_pk_bf16_f32 v9, v16, v17
	global_store_dwordx4 v[14:15], v[6:9], off offset:256
	v_pk_fma_f32 v[14:15], v[82:83], s[18:19], v[18:19] op_sel_hi:[1,0,1]
	v_readlane_b32 s72, v254, 4
	v_or_b32_e32 v6, 48, v10
	v_ashrrev_i32_e32 v7, 31, v6
	v_lshlrev_b64 v[6:7], 12, v[6:7]
	v_lshl_add_u64 v[6:7], s[8:9], 0, v[6:7]
	v_lshl_add_u64 v[10:11], v[6:7], 0, v[12:13]
	v_pk_fma_f32 v[8:9], v[88:89], s[18:19], v[24:25] op_sel_hi:[1,0,1]
	v_pk_fma_f32 v[6:7], v[86:87], s[18:19], v[22:23] op_sel_hi:[1,0,1]
	v_pk_fma_f32 v[12:13], v[84:85], s[18:19], v[20:21] op_sel_hi:[1,0,1]
	v_cvt_pk_bf16_f32 v6, v6, v7
	v_cvt_pk_bf16_f32 v7, v8, v9
	v_cvt_pk_bf16_f32 v8, v14, v15
	v_pk_fma_f32 v[14:15], v[90:91], s[18:19], v[26:27] op_sel_hi:[1,0,1]
	v_cvt_pk_bf16_f32 v9, v12, v13
	global_store_dwordx4 v[10:11], v[6:9], off
	v_pk_fma_f32 v[12:13], v[92:93], s[18:19], v[28:29] op_sel_hi:[1,0,1]
	v_readlane_b32 s73, v254, 5
	v_pk_fma_f32 v[8:9], v[96:97], s[18:19], v[32:33] op_sel_hi:[1,0,1]
	v_pk_fma_f32 v[6:7], v[94:95], s[18:19], v[30:31] op_sel_hi:[1,0,1]
	v_readlane_b32 s74, v254, 6
	v_cvt_pk_bf16_f32 v6, v6, v7
	v_cvt_pk_bf16_f32 v7, v8, v9
	v_cvt_pk_bf16_f32 v8, v14, v15
	v_cvt_pk_bf16_f32 v9, v12, v13
	global_store_dwordx4 v[10:11], v[6:9], off offset:256
	v_pk_fma_f32 v[12:13], v[104:105], s[18:19], v[20:21] op_sel_hi:[1,0,1]
	v_pk_fma_f32 v[14:15], v[102:103], s[18:19], v[18:19] op_sel_hi:[1,0,1]
	v_pk_fma_f32 v[8:9], v[112:113], s[18:19], v[24:25] op_sel_hi:[1,0,1]
	v_pk_fma_f32 v[6:7], v[110:111], s[18:19], v[22:23] op_sel_hi:[1,0,1]
	v_lshl_add_u64 v[10:11], v[2:3], 0, s[38:39]
	v_cvt_pk_bf16_f32 v6, v6, v7
	v_cvt_pk_bf16_f32 v7, v8, v9
	v_cvt_pk_bf16_f32 v8, v14, v15
	v_cvt_pk_bf16_f32 v9, v12, v13
	v_add_co_u32_e32 v12, vcc, s27, v2
	v_pk_fma_f32 v[14:15], v[98:99], s[18:19], v[26:27] op_sel_hi:[1,0,1]
	s_nop 0
	v_addc_co_u32_e32 v13, vcc, 0, v3, vcc
	global_store_dwordx4 v[12:13], v[6:9], off
	v_pk_fma_f32 v[12:13], v[100:101], s[18:19], v[28:29] op_sel_hi:[1,0,1]
	s_mov_b32 s27, 0x90000
	v_pk_fma_f32 v[8:9], v[108:109], s[18:19], v[32:33] op_sel_hi:[1,0,1]
	v_pk_fma_f32 v[6:7], v[106:107], s[18:19], v[30:31] op_sel_hi:[1,0,1]
	s_mov_b64 s[38:39], 0x90000
	v_cvt_pk_bf16_f32 v6, v6, v7
	v_cvt_pk_bf16_f32 v7, v8, v9
	v_cvt_pk_bf16_f32 v8, v14, v15
	v_cvt_pk_bf16_f32 v9, v12, v13
	global_store_dwordx4 v[10:11], v[6:9], off offset:256
	v_pk_fma_f32 v[12:13], v[72:73], s[18:19], v[20:21] op_sel_hi:[1,0,1]
	v_pk_fma_f32 v[14:15], v[70:71], s[18:19], v[18:19] op_sel_hi:[1,0,1]
	v_pk_fma_f32 v[8:9], v[80:81], s[18:19], v[24:25] op_sel_hi:[1,0,1]
	v_pk_fma_f32 v[6:7], v[78:79], s[18:19], v[22:23] op_sel_hi:[1,0,1]
	v_lshl_add_u64 v[10:11], v[2:3], 0, s[38:39]
	v_cvt_pk_bf16_f32 v6, v6, v7
	v_cvt_pk_bf16_f32 v7, v8, v9
	v_cvt_pk_bf16_f32 v8, v14, v15
	v_cvt_pk_bf16_f32 v9, v12, v13
	v_add_co_u32_e32 v12, vcc, s27, v2
	v_pk_fma_f32 v[14:15], v[66:67], s[18:19], v[26:27] op_sel_hi:[1,0,1]
	s_nop 0
	v_addc_co_u32_e32 v13, vcc, 0, v3, vcc
	global_store_dwordx4 v[12:13], v[6:9], off
	v_pk_fma_f32 v[12:13], v[68:69], s[18:19], v[28:29] op_sel_hi:[1,0,1]
	s_mov_b64 s[38:39], 0xa0000
	v_pk_fma_f32 v[8:9], v[76:77], s[18:19], v[32:33] op_sel_hi:[1,0,1]
	v_pk_fma_f32 v[6:7], v[74:75], s[18:19], v[30:31] op_sel_hi:[1,0,1]
	v_readlane_b32 s75, v254, 7
	v_cvt_pk_bf16_f32 v6, v6, v7
	v_cvt_pk_bf16_f32 v7, v8, v9
	v_cvt_pk_bf16_f32 v8, v14, v15
	v_cvt_pk_bf16_f32 v9, v12, v13
	global_store_dwordx4 v[10:11], v[6:9], off offset:256
	v_pk_fma_f32 v[12:13], v[56:57], s[18:19], v[20:21] op_sel_hi:[1,0,1]
	v_pk_fma_f32 v[14:15], v[54:55], s[18:19], v[18:19] op_sel_hi:[1,0,1]
	v_pk_fma_f32 v[8:9], v[64:65], s[18:19], v[24:25] op_sel_hi:[1,0,1]
	v_pk_fma_f32 v[6:7], v[62:63], s[18:19], v[22:23] op_sel_hi:[1,0,1]
	v_lshl_add_u64 v[10:11], v[2:3], 0, s[38:39]
	v_cvt_pk_bf16_f32 v6, v6, v7
	v_cvt_pk_bf16_f32 v7, v8, v9
	v_cvt_pk_bf16_f32 v8, v14, v15
	v_cvt_pk_bf16_f32 v9, v12, v13
	v_add_co_u32_e32 v12, vcc, s66, v2
	v_pk_fma_f32 v[14:15], v[50:51], s[18:19], v[26:27] op_sel_hi:[1,0,1]
	s_nop 0
	v_addc_co_u32_e32 v13, vcc, 0, v3, vcc
	global_store_dwordx4 v[12:13], v[6:9], off
	v_pk_fma_f32 v[12:13], v[52:53], s[18:19], v[28:29] op_sel_hi:[1,0,1]
	s_mov_b64 s[38:39], -1
	v_pk_fma_f32 v[8:9], v[60:61], s[18:19], v[32:33] op_sel_hi:[1,0,1]
	v_pk_fma_f32 v[6:7], v[58:59], s[18:19], v[30:31] op_sel_hi:[1,0,1]
	s_nop 0
	v_cvt_pk_bf16_f32 v6, v6, v7
	v_cvt_pk_bf16_f32 v7, v8, v9
	v_cvt_pk_bf16_f32 v8, v14, v15
	v_cvt_pk_bf16_f32 v9, v12, v13
	global_store_dwordx4 v[10:11], v[6:9], off offset:256
	v_lshl_add_u64 v[10:11], v[2:3], 0, s[20:21]
	v_add_co_u32_e32 v2, vcc, s67, v2
	v_pk_fma_f32 v[8:9], v[48:49], s[18:19], v[24:25] op_sel_hi:[1,0,1]
	v_pk_fma_f32 v[6:7], v[46:47], s[18:19], v[22:23] op_sel_hi:[1,0,1]
	v_pk_fma_f32 v[12:13], v[44:45], s[18:19], v[20:21] op_sel_hi:[1,0,1]
	v_pk_fma_f32 v[14:15], v[42:43], s[18:19], v[18:19] op_sel_hi:[1,0,1]
	v_cvt_pk_bf16_f32 v6, v6, v7
	v_cvt_pk_bf16_f32 v7, v8, v9
	v_addc_co_u32_e32 v3, vcc, 0, v3, vcc
	v_cvt_pk_bf16_f32 v8, v14, v15
	v_cvt_pk_bf16_f32 v9, v12, v13
	global_store_dwordx4 v[2:3], v[6:9], off
	s_and_b64 vcc, s[42:43], exec
	v_pk_fma_f32 v[2:3], v[40:41], s[18:19], v[32:33] op_sel_hi:[1,0,1]
	v_pk_fma_f32 v[6:7], v[38:39], s[18:19], v[30:31] op_sel_hi:[1,0,1]
	v_pk_fma_f32 v[8:9], v[34:35], s[18:19], v[26:27] op_sel_hi:[1,0,1]
	v_pk_fma_f32 v[12:13], v[36:37], s[18:19], v[28:29] op_sel_hi:[1,0,1]
	v_cvt_pk_bf16_f32 v6, v6, v7
	v_cvt_pk_bf16_f32 v7, v2, v3
	v_cvt_pk_bf16_f32 v8, v8, v9
	s_nop 0
	v_cvt_pk_bf16_f32 v9, v12, v13
	global_store_dwordx4 v[10:11], v[6:9], off offset:256
	s_cbranch_vccz .LBB0_1541
	s_lshl_b32 s27, s24, 8
	s_or_b32 s25, s25, s27
	v_or_b32_e32 v2, s25, v4
	v_ashrrev_i32_e32 v3, 31, v2
	v_mov_b32_e32 v18, 0
	s_and_b64 vcc, exec, s[6:7]
	v_mov_b32_e32 v22, 0
	v_mov_b32_e32 v23, 0
	v_mov_b32_e32 v24, 0
	v_mov_b32_e32 v25, 0
	s_cbranch_vccnz .LBB0_1551
	s_ashr_i32 s27, s26, 31
	s_lshl_b64 s[38:39], s[26:27], 13
	s_add_u32 s38, s68, s38
	s_addc_u32 s39, s69, s39
	v_lshl_add_u64 v[4:5], v[2:3], 2, s[38:39]
	global_load_dwordx4 v[22:25], v[4:5], off
